# A/B: the four GEMM k-loops without per-phase priority flips, one static raise for waves 4-7 per GEMM phase
# speedup vs baseline: 1.0034x; 1.0034x over previous
; #define PG8_STAGE(bufoff, gbase, voff) do { _Pragma("unroll") for (int _i = 0; _i < 2; ++_i) \
;         __builtin_amdgcn_global_load_lds((const unsigned*)((const char*)(gbase) + (voff)[_i]), (LAS unsigned*)(lds + (bufoff) + ldsw + _i * 8192), 16, 0, 0); } while (0)
; #define PG8_LDA(dst, b, h) do { _Pragma("unroll") for (int m = 0; m < 4; ++m) _Pragma("unroll") for (int k = 0; k < 2; ++k) dst[m][k] = *(const LAS bf16x8*)(lds + PG8_SA(b, h) + aoff + m * 2048 + k * 1024); } while (0)
; #define PG8_LDB(dst, b, h) do { _Pragma("unroll") for (int n = 0; n < 2; ++n) _Pragma("unroll") for (int k = 0; k < 2; ++k) dst[n][k] = *(const LAS bf16x8*)(lds + PG8_SB(b, h) + boff + n * 2048 + k * 1024); } while (0)
; #define PG8_MMA(ai, bj, At, Bt) do { __builtin_amdgcn_s_setprio(1); _Pragma("unroll") for (int m = 0; m < 4; ++m) _Pragma("unroll") for (int n = 0; n < 2; ++n) _Pragma("unroll") for (int k = 0; k < 2; ++k) \
;         acc[ai][bj][m][n] = __builtin_amdgcn_mfma_f32_16x16x32_bf16(Bt[n][k], At[m][k], acc[ai][bj][m][n], 0, 0, 0); __builtin_amdgcn_s_setprio(0); } while (0)
; #define PG8_WAIT_V(n) asm volatile("s_waitcnt vmcnt(" #n ")" ::: "memory")
; #define PG8_WAIT_L(n) asm volatile("s_waitcnt lgkmcnt(" #n ")" ::: "memory")
; #define PG8_BAR __builtin_amdgcn_s_barrier()
; #define PG8_SCHED __builtin_amdgcn_sched_barrier(0)
; template <class Epi, class Sched, bool ALIGN_EPI = true, bool SP2 = true>
; __device__ __forceinline__ void gemm_phase(LAS unsigned char* lds, const Dims g, const Sched& S, const Epi& E) {
;     ...
;             PG8_LDB(B0, 0, 0); PG8_LDB(B1, 0, 1); PG8_SCHED; PG8_LDA(At, 0, 0); PG8_STAGE(PG8_SA(1, 1), a1 + hstepA, voffA);
;             PG8_WAIT_V(8); PG8_WAIT_L(0); PG8_BAR; PG8_MMA(0, 0, At, B0); PG8_MMA(0, 1, At, B1); PG8_BAR; PG8_SCHED;
;             PG8_LDA(At, 0, 1); PG8_STAGE(PG8_SB(0, 0), b2, voffB); PG8_STAGE(PG8_SB(0, 1), b2 + hstepB, voffB); PG8_STAGE(PG8_SA(0, 0), a2, voffA);
;             PG8_WAIT_V(8); PG8_WAIT_L(0); PG8_BAR; PG8_MMA(1, 0, At, B0); PG8_MMA(1, 1, At, B1); PG8_BAR; PG8_SCHED;
.LBB0_326:
	s_add_u32 s35, s40, 0xfff80080
	s_addc_u32 s46, s41, -1
	s_add_i32 s61, 0, 0x10000
	s_cmp_eq_u32 s31, 28
	s_cselect_b32 s49, s37, s46
	s_cselect_b32 s48, s36, s35
	s_cselect_b32 s47, s45, s3
	s_cselect_b32 s46, s44, s2
	s_add_i32 s35, 0, 0x14000
	v_add_u32_e32 v144, s61, v163
	v_add_u32_e32 v164, s35, v163
	ds_read_b128 v[132:135], v144
	ds_read_b128 v[136:139], v144 offset:1024
	ds_read_b128 v[140:143], v144 offset:2048
	ds_read_b128 v[144:147], v144 offset:3072
	ds_read_b128 v[158:161], v164
	ds_read_b128 v[174:177], v164 offset:1024
	ds_read_b128 v[178:181], v164 offset:2048
	ds_read_b128 v[182:185], v164 offset:3072
	v_lshl_add_u64 v[164:165], s[40:41], 0, v[154:155]
	s_add_i32 m0, s43, 0xc000
	ds_read_b128 v[186:189], v173
	ds_read_b128 v[190:193], v173 offset:1024
	ds_read_b128 v[194:197], v173 offset:2048
	ds_read_b128 v[198:201], v173 offset:3072
	ds_read_b128 v[202:205], v173 offset:4096
	ds_read_b128 v[206:209], v173 offset:5120
	ds_read_b128 v[210:213], v173 offset:6144
	ds_read_b128 v[214:217], v173 offset:7168
	global_load_lds_dwordx4 v[164:165], off
	v_lshl_add_u64 v[164:165], s[40:41], 0, v[156:157]
	s_add_i32 m0, s43, 0xe000
	s_nop 0
	global_load_lds_dwordx4 v[164:165], off
	s_waitcnt vmcnt(8)
	s_waitcnt lgkmcnt(0)
	s_barrier
	s_waitcnt lgkmcnt(0)
	v_mfma_f32_16x16x32_bf16 v[128:131], v[132:135], v[186:189], v[128:131]
	v_mfma_f32_16x16x32_bf16 v[124:127], v[140:143], v[186:189], v[124:127]
	v_mfma_f32_16x16x32_bf16 v[116:119], v[132:135], v[194:197], v[116:119]
	v_mfma_f32_16x16x32_bf16 v[112:115], v[140:143], v[194:197], v[112:115]
	v_mfma_f32_16x16x32_bf16 v[104:107], v[132:135], v[202:205], v[104:107]
	v_mfma_f32_16x16x32_bf16 v[96:99], v[140:143], v[202:205], v[96:99]
	v_mfma_f32_16x16x32_bf16 v[86:89], v[132:135], v[210:213], v[86:89]
	v_mfma_f32_16x16x32_bf16 v[78:81], v[140:143], v[210:213], v[78:81]
	v_mfma_f32_16x16x32_bf16 v[128:131], v[136:139], v[190:193], v[128:131]
	v_mfma_f32_16x16x32_bf16 v[124:127], v[144:147], v[190:193], v[124:127]
	v_mfma_f32_16x16x32_bf16 v[116:119], v[136:139], v[198:201], v[116:119]
	v_mfma_f32_16x16x32_bf16 v[112:115], v[144:147], v[198:201], v[112:115]
	v_mfma_f32_16x16x32_bf16 v[104:107], v[136:139], v[206:209], v[104:107]
	v_mfma_f32_16x16x32_bf16 v[96:99], v[144:147], v[206:209], v[96:99]
	v_mfma_f32_16x16x32_bf16 v[86:89], v[136:139], v[214:217], v[86:89]
	v_mfma_f32_16x16x32_bf16 v[78:81], v[144:147], v[214:217], v[78:81]
	v_mfma_f32_16x16x32_bf16 v[120:123], v[158:161], v[186:189], v[120:123]
	v_mfma_f32_16x16x32_bf16 v[108:111], v[178:181], v[186:189], v[108:111]
	v_mfma_f32_16x16x32_bf16 v[100:103], v[158:161], v[194:197], v[100:103]
	v_mfma_f32_16x16x32_bf16 v[92:95], v[178:181], v[194:197], v[92:95]
	v_mfma_f32_16x16x32_bf16 v[82:85], v[158:161], v[202:205], v[82:85]
	v_mfma_f32_16x16x32_bf16 v[74:77], v[178:181], v[202:205], v[74:77]
	v_mfma_f32_16x16x32_bf16 v[70:73], v[158:161], v[210:213], v[70:73]
	v_mfma_f32_16x16x32_bf16 v[66:69], v[178:181], v[210:213], v[66:69]
	v_mfma_f32_16x16x32_bf16 v[120:123], v[174:177], v[190:193], v[120:123]
	v_mfma_f32_16x16x32_bf16 v[108:111], v[182:185], v[190:193], v[108:111]
	v_mfma_f32_16x16x32_bf16 v[100:103], v[174:177], v[198:201], v[100:103]
	v_mfma_f32_16x16x32_bf16 v[92:95], v[182:185], v[198:201], v[92:95]
	v_mfma_f32_16x16x32_bf16 v[82:85], v[174:177], v[206:209], v[82:85]
	v_mfma_f32_16x16x32_bf16 v[74:77], v[182:185], v[206:209], v[74:77]
	v_mfma_f32_16x16x32_bf16 v[70:73], v[174:177], v[214:217], v[70:73]
	v_mfma_f32_16x16x32_bf16 v[66:69], v[182:185], v[214:217], v[66:69]
	s_barrier
	s_add_i32 s61, s61, s52
	v_lshl_add_u64 v[164:165], s[46:47], 0, v[90:91]
	s_mov_b32 m0, s61
	ds_read_b128 v[186:189], v173 offset:16384
	ds_read_b128 v[190:193], v173 offset:17408
	ds_read_b128 v[194:197], v173 offset:18432
	ds_read_b128 v[198:201], v173 offset:19456
	ds_read_b128 v[202:205], v173 offset:20480
	ds_read_b128 v[206:209], v173 offset:21504
	ds_read_b128 v[210:213], v173 offset:22528
	ds_read_b128 v[214:217], v173 offset:23552
	global_load_lds_dwordx4 v[164:165], off
	s_add_i32 m0, s61, 0x2000
	s_add_u32 s62, s46, 0x80000
	v_lshl_add_u64 v[166:167], s[46:47], 0, v[152:153]
	s_addc_u32 s63, s47, 0
	s_add_i32 s35, s35, s52
	global_load_lds_dwordx4 v[166:167], off
	v_lshl_add_u64 v[234:235], s[62:63], 0, v[90:91]
	s_mov_b32 m0, s35
	v_lshl_add_u64 v[236:237], s[48:49], 0, v[150:151]
	global_load_lds_dwordx4 v[234:235], off
	v_lshl_add_u64 v[234:235], s[62:63], 0, v[152:153]
	s_add_i32 m0, s35, 0x2000
	s_nop 0
	global_load_lds_dwordx4 v[234:235], off
	v_lshl_add_u64 v[234:235], s[48:49], 0, v[148:149]
	s_mov_b32 m0, s43
	s_nop 0
	global_load_lds_dwordx4 v[234:235], off
	s_mov_b32 m0, s53
	s_nop 0
	global_load_lds_dwordx4 v[236:237], off
	s_waitcnt vmcnt(8)
	s_waitcnt lgkmcnt(0)
	s_barrier
; #define PG8_STAGE(bufoff, gbase, voff) do { _Pragma("unroll") for (int _i = 0; _i < 2; ++_i) \
;         __builtin_amdgcn_global_load_lds((const unsigned*)((const char*)(gbase) + (voff)[_i]), (LAS unsigned*)(lds + (bufoff) + ldsw + _i * 8192), 16, 0, 0); } while (0)
; #define PG8_LDA(dst, b, h) do { _Pragma("unroll") for (int m = 0; m < 4; ++m) _Pragma("unroll") for (int k = 0; k < 2; ++k) dst[m][k] = *(const LAS bf16x8*)(lds + PG8_SA(b, h) + aoff + m * 2048 + k * 1024); } while (0)
; #define PG8_LDB(dst, b, h) do { _Pragma("unroll") for (int n = 0; n < 2; ++n) _Pragma("unroll") for (int k = 0; k < 2; ++k) dst[n][k] = *(const LAS bf16x8*)(lds + PG8_SB(b, h) + boff + n * 2048 + k * 1024); } while (0)
; #define PG8_MMA(ai, bj, At, Bt) do { __builtin_amdgcn_s_setprio(1); _Pragma("unroll") for (int m = 0; m < 4; ++m) _Pragma("unroll") for (int n = 0; n < 2; ++n) _Pragma("unroll") for (int k = 0; k < 2; ++k) \
;         acc[ai][bj][m][n] = __builtin_amdgcn_mfma_f32_16x16x32_bf16(Bt[n][k], At[m][k], acc[ai][bj][m][n], 0, 0, 0); __builtin_amdgcn_s_setprio(0); } while (0)
; #define PG8_WAIT_V(n) asm volatile("s_waitcnt vmcnt(" #n ")" ::: "memory")
; #define PG8_WAIT_L(n) asm volatile("s_waitcnt lgkmcnt(" #n ")" ::: "memory")
; #define PG8_BAR __builtin_amdgcn_s_barrier()
; #define PG8_SCHED __builtin_amdgcn_sched_barrier(0)
; template <class Epi, class Sched, bool ALIGN_EPI = true, bool SP2 = true>
; __device__ __forceinline__ void gemm_phase(LAS unsigned char* lds, const Dims g, const Sched& S, const Epi& E) {
;     ...
;             PG8_WAIT_V(8); PG8_WAIT_L(0); PG8_BAR; PG8_MMA(1, 0, At, B0); PG8_MMA(1, 1, At, B1); PG8_BAR; PG8_SCHED;
;             PG8_LDB(B0, 1, 0); PG8_LDB(B1, 1, 1); PG8_SCHED; PG8_LDA(At, 1, 0); PG8_STAGE(PG8_SA(0, 1), a2 + hstepA, voffA);
;             PG8_WAIT_V(8); PG8_WAIT_L(0); PG8_BAR; PG8_MMA(0, 0, At, B0); PG8_MMA(0, 1, At, B1); PG8_BAR; PG8_SCHED;
;             PG8_LDA(At, 1, 1); PG8_STAGE(PG8_SB(1, 0), b3, voffB); PG8_STAGE(PG8_SB(1, 1), b3 + hstepB, voffB); PG8_STAGE(PG8_SA(1, 0), a3, voffA);
	s_waitcnt lgkmcnt(0)
	v_mfma_f32_16x16x32_bf16 v[62:65], v[132:135], v[186:189], v[62:65]
	v_mfma_f32_16x16x32_bf16 v[58:61], v[140:143], v[186:189], v[58:61]
	v_mfma_f32_16x16x32_bf16 v[54:57], v[132:135], v[194:197], v[54:57]
	v_mfma_f32_16x16x32_bf16 v[46:49], v[140:143], v[194:197], v[46:49]
	v_mfma_f32_16x16x32_bf16 v[38:41], v[132:135], v[202:205], v[38:41]
	v_mfma_f32_16x16x32_bf16 v[30:33], v[140:143], v[202:205], v[30:33]
	v_mfma_f32_16x16x32_bf16 v[22:25], v[132:135], v[210:213], v[22:25]
	v_mfma_f32_16x16x32_bf16 v[14:17], v[140:143], v[210:213], v[14:17]
	v_mfma_f32_16x16x32_bf16 v[62:65], v[136:139], v[190:193], v[62:65]
	v_mfma_f32_16x16x32_bf16 v[58:61], v[144:147], v[190:193], v[58:61]
	v_mfma_f32_16x16x32_bf16 v[54:57], v[136:139], v[198:201], v[54:57]
	v_mfma_f32_16x16x32_bf16 v[46:49], v[144:147], v[198:201], v[46:49]
	v_mfma_f32_16x16x32_bf16 v[38:41], v[136:139], v[206:209], v[38:41]
	v_mfma_f32_16x16x32_bf16 v[30:33], v[144:147], v[206:209], v[30:33]
	v_mfma_f32_16x16x32_bf16 v[22:25], v[136:139], v[214:217], v[22:25]
	v_mfma_f32_16x16x32_bf16 v[14:17], v[144:147], v[214:217], v[14:17]
	v_mfma_f32_16x16x32_bf16 v[50:53], v[158:161], v[186:189], v[50:53]
	v_mfma_f32_16x16x32_bf16 v[42:45], v[178:181], v[186:189], v[42:45]
	v_mfma_f32_16x16x32_bf16 v[34:37], v[158:161], v[194:197], v[34:37]
	v_mfma_f32_16x16x32_bf16 v[26:29], v[178:181], v[194:197], v[26:29]
	v_mfma_f32_16x16x32_bf16 v[18:21], v[158:161], v[202:205], v[18:21]
	v_mfma_f32_16x16x32_bf16 v[10:13], v[178:181], v[202:205], v[10:13]
	v_mfma_f32_16x16x32_bf16 v[6:9], v[158:161], v[210:213], v[6:9]
	v_mfma_f32_16x16x32_bf16 v[2:5], v[178:181], v[210:213], v[2:5]
	v_mfma_f32_16x16x32_bf16 v[50:53], v[174:177], v[190:193], v[50:53]
	v_mfma_f32_16x16x32_bf16 v[42:45], v[182:185], v[190:193], v[42:45]
	v_mfma_f32_16x16x32_bf16 v[34:37], v[174:177], v[198:201], v[34:37]
	v_mfma_f32_16x16x32_bf16 v[26:29], v[182:185], v[198:201], v[26:29]
	v_mfma_f32_16x16x32_bf16 v[18:21], v[174:177], v[206:209], v[18:21]
	v_mfma_f32_16x16x32_bf16 v[10:13], v[182:185], v[206:209], v[10:13]
	v_mfma_f32_16x16x32_bf16 v[6:9], v[174:177], v[214:217], v[6:9]
	v_mfma_f32_16x16x32_bf16 v[2:5], v[182:185], v[214:217], v[2:5]
	s_barrier
	s_add_i32 s35, 0, 0x18000
	s_add_i32 s61, 0, 0x1c000
	v_add_u32_e32 v144, s35, v163
	v_add_u32_e32 v182, s61, v163
	ds_read_b128 v[132:135], v144
	ds_read_b128 v[136:139], v144 offset:1024
	ds_read_b128 v[140:143], v144 offset:2048
	ds_read_b128 v[144:147], v144 offset:3072
	ds_read_b128 v[158:161], v182
	ds_read_b128 v[174:177], v182 offset:1024
	ds_read_b128 v[178:181], v182 offset:2048
	ds_read_b128 v[182:185], v182 offset:3072
	s_add_u32 s48, s48, 0x80000
	s_addc_u32 s49, s49, 0
	s_mov_b32 m0, s54
	v_lshl_add_u64 v[238:239], s[48:49], 0, v[148:149]
	ds_read_b128 v[186:189], v173 offset:32768
	ds_read_b128 v[190:193], v173 offset:33792
	ds_read_b128 v[194:197], v173 offset:34816
	ds_read_b128 v[198:201], v173 offset:35840
	ds_read_b128 v[202:205], v173 offset:36864
	ds_read_b128 v[206:209], v173 offset:37888
	ds_read_b128 v[210:213], v173 offset:38912
	ds_read_b128 v[214:217], v173 offset:39936
	global_load_lds_dwordx4 v[238:239], off
	v_lshl_add_u64 v[238:239], s[48:49], 0, v[150:151]
	s_mov_b32 m0, s55
	s_nop 0
	global_load_lds_dwordx4 v[238:239], off
	s_waitcnt vmcnt(8)
	s_waitcnt lgkmcnt(0)
	s_barrier
	s_waitcnt lgkmcnt(0)
	v_mfma_f32_16x16x32_bf16 v[128:131], v[132:135], v[186:189], v[128:131]
	v_mfma_f32_16x16x32_bf16 v[124:127], v[140:143], v[186:189], v[124:127]
	v_mfma_f32_16x16x32_bf16 v[116:119], v[132:135], v[194:197], v[116:119]
	v_mfma_f32_16x16x32_bf16 v[112:115], v[140:143], v[194:197], v[112:115]
	v_mfma_f32_16x16x32_bf16 v[104:107], v[132:135], v[202:205], v[104:107]
	v_mfma_f32_16x16x32_bf16 v[96:99], v[140:143], v[202:205], v[96:99]
	v_mfma_f32_16x16x32_bf16 v[86:89], v[132:135], v[210:213], v[86:89]
	v_mfma_f32_16x16x32_bf16 v[78:81], v[140:143], v[210:213], v[78:81]
	v_mfma_f32_16x16x32_bf16 v[128:131], v[136:139], v[190:193], v[128:131]
	v_mfma_f32_16x16x32_bf16 v[124:127], v[144:147], v[190:193], v[124:127]
	v_mfma_f32_16x16x32_bf16 v[116:119], v[136:139], v[198:201], v[116:119]
	v_mfma_f32_16x16x32_bf16 v[112:115], v[144:147], v[198:201], v[112:115]
	v_mfma_f32_16x16x32_bf16 v[104:107], v[136:139], v[206:209], v[104:107]
	v_mfma_f32_16x16x32_bf16 v[96:99], v[144:147], v[206:209], v[96:99]
	v_mfma_f32_16x16x32_bf16 v[86:89], v[136:139], v[214:217], v[86:89]
	v_mfma_f32_16x16x32_bf16 v[78:81], v[144:147], v[214:217], v[78:81]
	v_mfma_f32_16x16x32_bf16 v[120:123], v[158:161], v[186:189], v[120:123]
	v_mfma_f32_16x16x32_bf16 v[108:111], v[178:181], v[186:189], v[108:111]
	v_mfma_f32_16x16x32_bf16 v[100:103], v[158:161], v[194:197], v[100:103]
	v_mfma_f32_16x16x32_bf16 v[92:95], v[178:181], v[194:197], v[92:95]
	v_mfma_f32_16x16x32_bf16 v[82:85], v[158:161], v[202:205], v[82:85]
	v_mfma_f32_16x16x32_bf16 v[74:77], v[178:181], v[202:205], v[74:77]
	v_mfma_f32_16x16x32_bf16 v[70:73], v[158:161], v[210:213], v[70:73]
	v_mfma_f32_16x16x32_bf16 v[66:69], v[178:181], v[210:213], v[66:69]
	v_mfma_f32_16x16x32_bf16 v[120:123], v[174:177], v[190:193], v[120:123]
	v_mfma_f32_16x16x32_bf16 v[108:111], v[182:185], v[190:193], v[108:111]
	v_mfma_f32_16x16x32_bf16 v[100:103], v[174:177], v[198:201], v[100:103]
	v_mfma_f32_16x16x32_bf16 v[92:95], v[182:185], v[198:201], v[92:95]
	v_mfma_f32_16x16x32_bf16 v[82:85], v[174:177], v[206:209], v[82:85]
	v_mfma_f32_16x16x32_bf16 v[74:77], v[182:185], v[206:209], v[74:77]
	v_mfma_f32_16x16x32_bf16 v[70:73], v[174:177], v[214:217], v[70:73]
	v_mfma_f32_16x16x32_bf16 v[66:69], v[182:185], v[214:217], v[66:69]
	s_barrier
; #define PG8_STAGE(bufoff, gbase, voff) do { _Pragma("unroll") for (int _i = 0; _i < 2; ++_i) \
;         __builtin_amdgcn_global_load_lds((const unsigned*)((const char*)(gbase) + (voff)[_i]), (LAS unsigned*)(lds + (bufoff) + ldsw + _i * 8192), 16, 0, 0); } while (0)
; #define PG8_LDA(dst, b, h) do { _Pragma("unroll") for (int m = 0; m < 4; ++m) _Pragma("unroll") for (int k = 0; k < 2; ++k) dst[m][k] = *(const LAS bf16x8*)(lds + PG8_SA(b, h) + aoff + m * 2048 + k * 1024); } while (0)
; #define PG8_MMA(ai, bj, At, Bt) do { __builtin_amdgcn_s_setprio(1); _Pragma("unroll") for (int m = 0; m < 4; ++m) _Pragma("unroll") for (int n = 0; n < 2; ++n) _Pragma("unroll") for (int k = 0; k < 2; ++k) \
;         acc[ai][bj][m][n] = __builtin_amdgcn_mfma_f32_16x16x32_bf16(Bt[n][k], At[m][k], acc[ai][bj][m][n], 0, 0, 0); __builtin_amdgcn_s_setprio(0); } while (0)
; #define PG8_WAIT_V(n) asm volatile("s_waitcnt vmcnt(" #n ")" ::: "memory")
; #define PG8_WAIT_L(n) asm volatile("s_waitcnt lgkmcnt(" #n ")" ::: "memory")
; #define PG8_BAR __builtin_amdgcn_s_barrier()
; #define PG8_SCHED __builtin_amdgcn_sched_barrier(0)
; template <class Epi, class Sched, bool ALIGN_EPI = true, bool SP2 = true>
; __device__ __forceinline__ void gemm_phase(LAS unsigned char* lds, const Dims g, const Sched& S, const Epi& E) {
;     ...
;         for (int t = 0; t < nt; t += 2) {
;             const bool last = (t == nt - 2);
;             const char* a1 = cA + (size_t)(t + 1) * kstep;
;             const char* a2 = last ? nA : cA + (size_t)(t + 2) * kstep; const char* b2 = last ? nB : cB + (size_t)(t + 2) * kstep;
;             const char* a3 = a2 + kstep; const char* b3 = b2 + kstep;
;     ...
;             PG8_LDA(At, 1, 1); PG8_STAGE(PG8_SB(1, 0), b3, voffB); PG8_STAGE(PG8_SB(1, 1), b3 + hstepB, voffB); PG8_STAGE(PG8_SA(1, 0), a3, voffA);
;             PG8_WAIT_V(8); PG8_WAIT_L(0); PG8_BAR; PG8_MMA(1, 0, At, B0); PG8_MMA(1, 1, At, B1); PG8_BAR; PG8_SCHED;
	s_add_i32 s35, s35, s52
	v_lshl_add_u64 v[164:165], v[164:165], 0, s[16:17]
	s_mov_b32 m0, s35
	ds_read_b128 v[186:189], v173 offset:49152
	ds_read_b128 v[190:193], v173 offset:50176
	ds_read_b128 v[194:197], v173 offset:51200
	ds_read_b128 v[198:201], v173 offset:52224
	ds_read_b128 v[202:205], v173 offset:53248
	ds_read_b128 v[206:209], v173 offset:54272
	ds_read_b128 v[210:213], v173 offset:55296
	ds_read_b128 v[214:217], v173 offset:56320
	global_load_lds_dwordx4 v[164:165], off
	s_add_i32 m0, s35, 0x2000
	s_add_u32 s46, s46, 0x80080
	v_lshl_add_u64 v[164:165], v[166:167], 0, s[16:17]
	s_addc_u32 s47, s47, 0
	s_add_i32 s35, s61, s52
	global_load_lds_dwordx4 v[164:165], off
	v_lshl_add_u64 v[164:165], s[46:47], 0, v[90:91]
	s_mov_b32 m0, s35
	s_nop 0
	global_load_lds_dwordx4 v[164:165], off
	v_lshl_add_u64 v[164:165], s[46:47], 0, v[152:153]
	s_add_i32 m0, s35, 0x2000
	s_nop 0
	global_load_lds_dwordx4 v[164:165], off
	v_lshl_add_u64 v[164:165], v[234:235], 0, s[16:17]
	s_mov_b32 m0, s56
	s_nop 0
	global_load_lds_dwordx4 v[164:165], off
	v_lshl_add_u64 v[164:165], v[236:237], 0, s[16:17]
	s_mov_b32 m0, s57
	s_nop 0
	global_load_lds_dwordx4 v[164:165], off
	s_waitcnt vmcnt(8)
	s_waitcnt lgkmcnt(0)
	s_barrier
	s_waitcnt lgkmcnt(0)
	v_mfma_f32_16x16x32_bf16 v[62:65], v[132:135], v[186:189], v[62:65]
	v_mfma_f32_16x16x32_bf16 v[58:61], v[140:143], v[186:189], v[58:61]
	v_mfma_f32_16x16x32_bf16 v[54:57], v[132:135], v[194:197], v[54:57]
	v_mfma_f32_16x16x32_bf16 v[46:49], v[140:143], v[194:197], v[46:49]
	v_mfma_f32_16x16x32_bf16 v[38:41], v[132:135], v[202:205], v[38:41]
	v_mfma_f32_16x16x32_bf16 v[30:33], v[140:143], v[202:205], v[30:33]
	v_mfma_f32_16x16x32_bf16 v[22:25], v[132:135], v[210:213], v[22:25]
	v_mfma_f32_16x16x32_bf16 v[14:17], v[140:143], v[210:213], v[14:17]
	v_mfma_f32_16x16x32_bf16 v[62:65], v[136:139], v[190:193], v[62:65]
	v_mfma_f32_16x16x32_bf16 v[58:61], v[144:147], v[190:193], v[58:61]
	v_mfma_f32_16x16x32_bf16 v[54:57], v[136:139], v[198:201], v[54:57]
	v_mfma_f32_16x16x32_bf16 v[46:49], v[144:147], v[198:201], v[46:49]
	v_mfma_f32_16x16x32_bf16 v[38:41], v[136:139], v[206:209], v[38:41]
	v_mfma_f32_16x16x32_bf16 v[30:33], v[144:147], v[206:209], v[30:33]
	v_mfma_f32_16x16x32_bf16 v[22:25], v[136:139], v[214:217], v[22:25]
	v_mfma_f32_16x16x32_bf16 v[14:17], v[144:147], v[214:217], v[14:17]
	v_mfma_f32_16x16x32_bf16 v[50:53], v[158:161], v[186:189], v[50:53]
	v_mfma_f32_16x16x32_bf16 v[42:45], v[178:181], v[186:189], v[42:45]
	v_mfma_f32_16x16x32_bf16 v[34:37], v[158:161], v[194:197], v[34:37]
	v_mfma_f32_16x16x32_bf16 v[26:29], v[178:181], v[194:197], v[26:29]
	v_mfma_f32_16x16x32_bf16 v[18:21], v[158:161], v[202:205], v[18:21]
	v_mfma_f32_16x16x32_bf16 v[10:13], v[178:181], v[202:205], v[10:13]
	v_mfma_f32_16x16x32_bf16 v[6:9], v[158:161], v[210:213], v[6:9]
	v_mfma_f32_16x16x32_bf16 v[2:5], v[178:181], v[210:213], v[2:5]
	v_mfma_f32_16x16x32_bf16 v[50:53], v[174:177], v[190:193], v[50:53]
	v_mfma_f32_16x16x32_bf16 v[42:45], v[182:185], v[190:193], v[42:45]
	v_mfma_f32_16x16x32_bf16 v[34:37], v[174:177], v[198:201], v[34:37]
	v_mfma_f32_16x16x32_bf16 v[26:29], v[182:185], v[198:201], v[26:29]
	v_mfma_f32_16x16x32_bf16 v[18:21], v[174:177], v[206:209], v[18:21]
	v_mfma_f32_16x16x32_bf16 v[10:13], v[182:185], v[206:209], v[10:13]
	v_mfma_f32_16x16x32_bf16 v[6:9], v[174:177], v[214:217], v[6:9]
	v_mfma_f32_16x16x32_bf16 v[2:5], v[182:185], v[214:217], v[2:5]
	s_barrier
	s_add_i32 s31, s31, 2
	s_add_u32 s40, s40, 0x100
	s_addc_u32 s41, s41, 0
	s_add_u32 s2, s2, 0x100
	s_addc_u32 s3, s3, 0
	s_cmp_gt_u32 s31, 29
	s_cbranch_scc0 .LBB0_326
	s_and_b64 vcc, exec, s[26:27]
	s_cbranch_vccz .LBB0_329
	s_barrier

; #define IN(k) (((PHMASK >> PHBIT(k)) & 1u) && lo <= (k) && (k) < hi)
; #define SEAM(k) do { if (IN(k) && IN((k) + 1)) xcd_barrier(bar); } while (0)
; #define DUP(bit) if constexpr (((PROBE_DUP >> (bit)) & 1u) != 0u)
; #define RUN_GEMM1() { PH_BEGIN(); pg8::RectOrder S; S.init(ws + WS_U, (const bf16*)(ws + WS_W1T) + (size_t)l * NZ * D, D, D, TP / 256, NZ / 256, G, bid); \
;             pg8::EpiBf16 E{(bf16*)(ws + WS_Z), NZ, (const float*)(ws + WS_BIAS) + (size_t)l * NZ}; \
;             pg8::gemm_phase<pg8::EpiBf16, pg8::RectOrder>(lds, pg8::Dims{D, D, D / 64}, S, E); }
; __global__ void __launch_bounds__(NTHR, 2) mk_fwd(ArgsV argsv) {
;     ...
;         if (IN(pb + 1)) { RUN_GEMM1(); DUP(PB_GEMM1) RUN_GEMM1();
;             { PH_BEGIN(); const int nfull = (TP / 256) * (NZ / 256) % G;
;               if (l == 0) { if (nfull != 0 && bid >= nfull) phase_convert<0>(a, 1, lds, (bid - nfull) * NWAVES + wave, (G - nfull) * NWAVES, wave, lane); else if (nfull == 0) phase_convert<0>(a, 1, lds, gw, NGW, wave, lane); }
;               else        { if (nfull != 0 && bid >= nfull) phase_convert<1>(a, 1, lds, (bid - nfull) * NWAVES + wave, (G - nfull) * NWAVES, wave, lane); else if (nfull == 0) phase_convert<1>(a, 1, lds, gw, NGW, wave, lane); } } } SEAM(pb + 1);
;         if (IN(pb + 2)) { { PH_BEGIN(); phase_rope(a, gw, NGW, lane); } { PH_BEGIN(); phase_vt(a, gw, NGW, lane); } DUP(PB_VT) { PH_BEGIN(); phase_vt(a, gw, NGW, lane); }
;             { PH_BEGIN(); phase_rwkvprep(a, l, lds, tid, gw, NGW, lane); } DUP(PB_RWKVPREP) { PH_BEGIN(); phase_rwkvprep(a, l, lds, tid, gw, NGW, lane); } } SEAM(pb + 2);
.LBB0_784:
	s_setprio 0
	s_cmp_le_i32 s76, s0
	s_cselect_b64 s[2:3], -1, 0
	s_cmp_lt_i32 s0, s77
	s_cselect_b64 s[0:1], -1, 0
	s_and_b64 s[0:1], s[2:3], s[0:1]
	s_mov_b64 s[2:3], -1
	s_and_b64 vcc, exec, s[0:1]
	s_cbranch_vccnz .LBB0_786
	v_readlane_b32 s0, v255, 30
	s_mul_i32 s0, s0, 10
	s_add_i32 s0, s0, 4
	s_mov_b64 s[2:3], 0
	v_readlane_b32 s1, v255, 31

; #define PG8_STAGE(bufoff, gbase, voff) do { _Pragma("unroll") for (int _i = 0; _i < 2; ++_i) \
;         __builtin_amdgcn_global_load_lds((const unsigned*)((const char*)(gbase) + (voff)[_i]), (LAS unsigned*)(lds + (bufoff) + ldsw + _i * 8192), 16, 0, 0); } while (0)
; #define PG8_LDA(dst, b, h) do { _Pragma("unroll") for (int m = 0; m < 4; ++m) _Pragma("unroll") for (int k = 0; k < 2; ++k) dst[m][k] = *(const LAS bf16x8*)(lds + PG8_SA(b, h) + aoff + m * 2048 + k * 1024); } while (0)
; #define PG8_LDB(dst, b, h) do { _Pragma("unroll") for (int n = 0; n < 2; ++n) _Pragma("unroll") for (int k = 0; k < 2; ++k) dst[n][k] = *(const LAS bf16x8*)(lds + PG8_SB(b, h) + boff + n * 2048 + k * 1024); } while (0)
; #define PG8_MMA(ai, bj, At, Bt) do { __builtin_amdgcn_s_setprio(1); _Pragma("unroll") for (int m = 0; m < 4; ++m) _Pragma("unroll") for (int n = 0; n < 2; ++n) _Pragma("unroll") for (int k = 0; k < 2; ++k) \
;         acc[ai][bj][m][n] = __builtin_amdgcn_mfma_f32_16x16x32_bf16(Bt[n][k], At[m][k], acc[ai][bj][m][n], 0, 0, 0); __builtin_amdgcn_s_setprio(0); } while (0)
; #define PG8_WAIT_V(n) asm volatile("s_waitcnt vmcnt(" #n ")" ::: "memory")
; #define PG8_WAIT_L(n) asm volatile("s_waitcnt lgkmcnt(" #n ")" ::: "memory")
; #define PG8_BAR __builtin_amdgcn_s_barrier()
; #define PG8_SCHED __builtin_amdgcn_sched_barrier(0)
; template <class Epi, class Sched, bool ALIGN_EPI = true, bool SP2 = true>
; __device__ __forceinline__ void gemm_phase(LAS unsigned char* lds, const Dims g, const Sched& S, const Epi& E) {
;     ...
;             PG8_LDB(B0, 0, 0); PG8_LDB(B1, 0, 1); PG8_SCHED; PG8_LDA(At, 0, 0); PG8_STAGE(PG8_SA(1, 1), a1 + hstepA, voffA);
;             PG8_WAIT_V(8); PG8_WAIT_L(0); PG8_BAR; PG8_MMA(0, 0, At, B0); PG8_MMA(0, 1, At, B1); PG8_BAR; PG8_SCHED;
;             PG8_LDA(At, 0, 1); PG8_STAGE(PG8_SB(0, 0), b2, voffB); PG8_STAGE(PG8_SB(0, 1), b2 + hstepB, voffB); PG8_STAGE(PG8_SA(0, 0), a2, voffA);
;             PG8_WAIT_V(8); PG8_WAIT_L(0); PG8_BAR; PG8_MMA(1, 0, At, B0); PG8_MMA(1, 1, At, B1); PG8_BAR; PG8_SCHED;
.LBB0_1402:
	s_add_u32 s4, s24, 0xfffc0080
	s_addc_u32 s5, s25, -1
	s_add_i32 s33, 0, 0x10000
	s_cmp_eq_u32 s3, 12
	s_cselect_b32 s29, s55, s5
	s_cselect_b32 s28, s54, s4
	s_cselect_b32 s27, s57, s2
	s_cselect_b32 s26, s56, s1
	s_add_i32 s51, 0, 0x14000
	v_add_u32_e32 v154, s33, v160
	v_add_u32_e32 v163, s51, v160
	ds_read_b128 v[128:131], v154
	ds_read_b128 v[136:139], v154 offset:1024
	ds_read_b128 v[150:153], v154 offset:2048
	ds_read_b128 v[154:157], v154 offset:3072
	ds_read_b128 v[172:175], v163
	ds_read_b128 v[176:179], v163 offset:1024
	ds_read_b128 v[180:183], v163 offset:2048
	ds_read_b128 v[184:187], v163 offset:3072
	v_lshl_add_u64 v[164:165], s[24:25], 0, v[146:147]
	s_add_i32 m0, s13, 0xc000
	ds_read_b128 v[188:191], v162
	ds_read_b128 v[192:195], v162 offset:1024
	ds_read_b128 v[196:199], v162 offset:2048
	ds_read_b128 v[200:203], v162 offset:3072
	ds_read_b128 v[204:207], v162 offset:4096
	ds_read_b128 v[208:211], v162 offset:5120
	ds_read_b128 v[212:215], v162 offset:6144
	ds_read_b128 v[234:237], v162 offset:7168
	global_load_lds_dwordx4 v[164:165], off
	v_lshl_add_u64 v[164:165], s[24:25], 0, v[148:149]
	s_add_i32 m0, s13, 0xe000
	s_nop 0
	global_load_lds_dwordx4 v[164:165], off
	s_waitcnt vmcnt(8)
	s_waitcnt lgkmcnt(0)
	s_barrier
	s_waitcnt lgkmcnt(0)
	v_mfma_f32_16x16x32_bf16 v[132:135], v[128:131], v[188:191], v[132:135]
	v_mfma_f32_16x16x32_bf16 v[124:127], v[150:153], v[188:191], v[124:127]
	v_mfma_f32_16x16x32_bf16 v[112:115], v[128:131], v[196:199], v[112:115]
	v_mfma_f32_16x16x32_bf16 v[108:111], v[150:153], v[196:199], v[108:111]
	v_mfma_f32_16x16x32_bf16 v[96:99], v[128:131], v[204:207], v[96:99]
	v_mfma_f32_16x16x32_bf16 v[92:95], v[150:153], v[204:207], v[92:95]
	v_mfma_f32_16x16x32_bf16 v[78:81], v[128:131], v[212:215], v[78:81]
	v_mfma_f32_16x16x32_bf16 v[74:77], v[150:153], v[212:215], v[74:77]
	v_mfma_f32_16x16x32_bf16 v[132:135], v[136:139], v[192:195], v[132:135]
	v_mfma_f32_16x16x32_bf16 v[124:127], v[154:157], v[192:195], v[124:127]
	v_mfma_f32_16x16x32_bf16 v[112:115], v[136:139], v[200:203], v[112:115]
	v_mfma_f32_16x16x32_bf16 v[108:111], v[154:157], v[200:203], v[108:111]
	v_mfma_f32_16x16x32_bf16 v[96:99], v[136:139], v[208:211], v[96:99]
	v_mfma_f32_16x16x32_bf16 v[92:95], v[154:157], v[208:211], v[92:95]
	v_mfma_f32_16x16x32_bf16 v[78:81], v[136:139], v[234:237], v[78:81]
	v_mfma_f32_16x16x32_bf16 v[74:77], v[154:157], v[234:237], v[74:77]
	v_mfma_f32_16x16x32_bf16 v[120:123], v[172:175], v[188:191], v[120:123]
	v_mfma_f32_16x16x32_bf16 v[116:119], v[180:183], v[188:191], v[116:119]
	v_mfma_f32_16x16x32_bf16 v[104:107], v[172:175], v[196:199], v[104:107]
	v_mfma_f32_16x16x32_bf16 v[100:103], v[180:183], v[196:199], v[100:103]
	v_mfma_f32_16x16x32_bf16 v[86:89], v[172:175], v[204:207], v[86:89]
	v_mfma_f32_16x16x32_bf16 v[82:85], v[180:183], v[204:207], v[82:85]
	v_mfma_f32_16x16x32_bf16 v[70:73], v[172:175], v[212:215], v[70:73]
	v_mfma_f32_16x16x32_bf16 v[66:69], v[180:183], v[212:215], v[66:69]
	v_mfma_f32_16x16x32_bf16 v[120:123], v[176:179], v[192:195], v[120:123]
	v_mfma_f32_16x16x32_bf16 v[116:119], v[184:187], v[192:195], v[116:119]
	v_mfma_f32_16x16x32_bf16 v[104:107], v[176:179], v[200:203], v[104:107]
	v_mfma_f32_16x16x32_bf16 v[100:103], v[184:187], v[200:203], v[100:103]
	v_mfma_f32_16x16x32_bf16 v[86:89], v[176:179], v[208:211], v[86:89]
	v_mfma_f32_16x16x32_bf16 v[82:85], v[184:187], v[208:211], v[82:85]
	v_mfma_f32_16x16x32_bf16 v[70:73], v[176:179], v[234:237], v[70:73]
	v_mfma_f32_16x16x32_bf16 v[66:69], v[184:187], v[234:237], v[66:69]
	s_barrier
	s_add_i32 s4, s33, s37
	v_lshl_add_u64 v[164:165], s[26:27], 0, v[90:91]
	s_mov_b32 m0, s4
	ds_read_b128 v[188:191], v162 offset:16384
	ds_read_b128 v[192:195], v162 offset:17408
	ds_read_b128 v[196:199], v162 offset:18432
	ds_read_b128 v[200:203], v162 offset:19456
	ds_read_b128 v[204:207], v162 offset:20480
	ds_read_b128 v[208:211], v162 offset:21504
	ds_read_b128 v[212:215], v162 offset:22528
	ds_read_b128 v[234:237], v162 offset:23552
	global_load_lds_dwordx4 v[164:165], off
	s_add_i32 m0, s4, 0x2000
	s_add_u32 s4, s26, 0x40000
	v_lshl_add_u64 v[166:167], s[26:27], 0, v[144:145]
	s_addc_u32 s5, s27, 0
	s_add_i32 s33, s51, s37
	global_load_lds_dwordx4 v[166:167], off
	v_lshl_add_u64 v[216:217], s[4:5], 0, v[90:91]
	s_mov_b32 m0, s33
	v_lshl_add_u64 v[238:239], s[28:29], 0, v[142:143]
	global_load_lds_dwordx4 v[216:217], off
	v_lshl_add_u64 v[216:217], s[4:5], 0, v[144:145]
	s_add_i32 m0, s33, 0x2000
	s_nop 0
	global_load_lds_dwordx4 v[216:217], off
	v_lshl_add_u64 v[216:217], s[28:29], 0, v[140:141]
	s_mov_b32 m0, s13
	s_nop 0
	global_load_lds_dwordx4 v[216:217], off
	s_mov_b32 m0, s58
	s_nop 0
	global_load_lds_dwordx4 v[238:239], off
	s_waitcnt vmcnt(8)
	s_waitcnt lgkmcnt(0)
	s_barrier
; #define PG8_STAGE(bufoff, gbase, voff) do { _Pragma("unroll") for (int _i = 0; _i < 2; ++_i) \
;         __builtin_amdgcn_global_load_lds((const unsigned*)((const char*)(gbase) + (voff)[_i]), (LAS unsigned*)(lds + (bufoff) + ldsw + _i * 8192), 16, 0, 0); } while (0)
; #define PG8_LDA(dst, b, h) do { _Pragma("unroll") for (int m = 0; m < 4; ++m) _Pragma("unroll") for (int k = 0; k < 2; ++k) dst[m][k] = *(const LAS bf16x8*)(lds + PG8_SA(b, h) + aoff + m * 2048 + k * 1024); } while (0)
; #define PG8_LDB(dst, b, h) do { _Pragma("unroll") for (int n = 0; n < 2; ++n) _Pragma("unroll") for (int k = 0; k < 2; ++k) dst[n][k] = *(const LAS bf16x8*)(lds + PG8_SB(b, h) + boff + n * 2048 + k * 1024); } while (0)
; #define PG8_MMA(ai, bj, At, Bt) do { __builtin_amdgcn_s_setprio(1); _Pragma("unroll") for (int m = 0; m < 4; ++m) _Pragma("unroll") for (int n = 0; n < 2; ++n) _Pragma("unroll") for (int k = 0; k < 2; ++k) \
;         acc[ai][bj][m][n] = __builtin_amdgcn_mfma_f32_16x16x32_bf16(Bt[n][k], At[m][k], acc[ai][bj][m][n], 0, 0, 0); __builtin_amdgcn_s_setprio(0); } while (0)
; #define PG8_WAIT_V(n) asm volatile("s_waitcnt vmcnt(" #n ")" ::: "memory")
; #define PG8_WAIT_L(n) asm volatile("s_waitcnt lgkmcnt(" #n ")" ::: "memory")
; #define PG8_BAR __builtin_amdgcn_s_barrier()
; template <class Epi, class Sched, bool ALIGN_EPI = true, bool SP2 = true>
; __device__ __forceinline__ void gemm_phase(LAS unsigned char* lds, const Dims g, const Sched& S, const Epi& E) {
;     ...
;             PG8_WAIT_V(8); PG8_WAIT_L(0); PG8_BAR; PG8_MMA(0, 0, At, B0); PG8_MMA(0, 1, At, B1); PG8_BAR; PG8_SCHED;
;             PG8_LDA(At, 0, 1); PG8_STAGE(PG8_SB(0, 0), b2, voffB); PG8_STAGE(PG8_SB(0, 1), b2 + hstepB, voffB); PG8_STAGE(PG8_SA(0, 0), a2, voffA);
;             PG8_WAIT_V(8); PG8_WAIT_L(0); PG8_BAR; PG8_MMA(1, 0, At, B0); PG8_MMA(1, 1, At, B1); PG8_BAR; PG8_SCHED;
;             PG8_LDB(B0, 1, 0); PG8_LDB(B1, 1, 1); PG8_SCHED; PG8_LDA(At, 1, 0); PG8_STAGE(PG8_SA(0, 1), a2 + hstepA, voffA);
;             PG8_WAIT_V(8); PG8_WAIT_L(0); PG8_BAR; PG8_MMA(0, 0, At, B0); PG8_MMA(0, 1, At, B1); PG8_BAR; PG8_SCHED;
;             PG8_LDA(At, 1, 1); PG8_STAGE(PG8_SB(1, 0), b3, voffB); PG8_STAGE(PG8_SB(1, 1), b3 + hstepB, voffB); PG8_STAGE(PG8_SA(1, 0), a3, voffA);
;             PG8_WAIT_V(8); PG8_WAIT_L(0); PG8_BAR; PG8_MMA(1, 0, At, B0); PG8_MMA(1, 1, At, B1); PG8_BAR; PG8_SCHED;
	s_waitcnt lgkmcnt(0)
	v_mfma_f32_16x16x32_bf16 v[62:65], v[128:131], v[188:191], v[62:65]
	v_mfma_f32_16x16x32_bf16 v[58:61], v[150:153], v[188:191], v[58:61]
	v_mfma_f32_16x16x32_bf16 v[46:49], v[128:131], v[196:199], v[46:49]
	v_mfma_f32_16x16x32_bf16 v[42:45], v[150:153], v[196:199], v[42:45]
	v_mfma_f32_16x16x32_bf16 v[30:33], v[128:131], v[204:207], v[30:33]
	v_mfma_f32_16x16x32_bf16 v[26:29], v[150:153], v[204:207], v[26:29]
	v_mfma_f32_16x16x32_bf16 v[14:17], v[128:131], v[212:215], v[14:17]
	v_mfma_f32_16x16x32_bf16 v[10:13], v[150:153], v[212:215], v[10:13]
	v_mfma_f32_16x16x32_bf16 v[62:65], v[136:139], v[192:195], v[62:65]
	v_mfma_f32_16x16x32_bf16 v[58:61], v[154:157], v[192:195], v[58:61]
	v_mfma_f32_16x16x32_bf16 v[46:49], v[136:139], v[200:203], v[46:49]
	v_mfma_f32_16x16x32_bf16 v[42:45], v[154:157], v[200:203], v[42:45]
	v_mfma_f32_16x16x32_bf16 v[30:33], v[136:139], v[208:211], v[30:33]
	v_mfma_f32_16x16x32_bf16 v[26:29], v[154:157], v[208:211], v[26:29]
	v_mfma_f32_16x16x32_bf16 v[14:17], v[136:139], v[234:237], v[14:17]
	v_mfma_f32_16x16x32_bf16 v[10:13], v[154:157], v[234:237], v[10:13]
	v_mfma_f32_16x16x32_bf16 v[54:57], v[172:175], v[188:191], v[54:57]
	v_mfma_f32_16x16x32_bf16 v[50:53], v[180:183], v[188:191], v[50:53]
	v_mfma_f32_16x16x32_bf16 v[38:41], v[172:175], v[196:199], v[38:41]
	v_mfma_f32_16x16x32_bf16 v[34:37], v[180:183], v[196:199], v[34:37]
	v_mfma_f32_16x16x32_bf16 v[22:25], v[172:175], v[204:207], v[22:25]
	v_mfma_f32_16x16x32_bf16 v[18:21], v[180:183], v[204:207], v[18:21]
	v_mfma_f32_16x16x32_bf16 v[6:9], v[172:175], v[212:215], v[6:9]
	v_mfma_f32_16x16x32_bf16 v[2:5], v[180:183], v[212:215], v[2:5]
	v_mfma_f32_16x16x32_bf16 v[54:57], v[176:179], v[192:195], v[54:57]
	v_mfma_f32_16x16x32_bf16 v[50:53], v[184:187], v[192:195], v[50:53]
	v_mfma_f32_16x16x32_bf16 v[38:41], v[176:179], v[200:203], v[38:41]
	v_mfma_f32_16x16x32_bf16 v[34:37], v[184:187], v[200:203], v[34:37]
	v_mfma_f32_16x16x32_bf16 v[22:25], v[176:179], v[208:211], v[22:25]
	v_mfma_f32_16x16x32_bf16 v[18:21], v[184:187], v[208:211], v[18:21]
	v_mfma_f32_16x16x32_bf16 v[6:9], v[176:179], v[234:237], v[6:9]
	v_mfma_f32_16x16x32_bf16 v[2:5], v[184:187], v[234:237], v[2:5]
	s_barrier
	s_add_i32 s33, 0, 0x18000
	s_add_i32 s51, 0, 0x1c000
	v_add_u32_e32 v154, s33, v160
	v_add_u32_e32 v163, s51, v160
	ds_read_b128 v[128:131], v154
	ds_read_b128 v[136:139], v154 offset:1024
	ds_read_b128 v[150:153], v154 offset:2048
	ds_read_b128 v[154:157], v154 offset:3072
	ds_read_b128 v[172:175], v163
	ds_read_b128 v[176:179], v163 offset:1024
	ds_read_b128 v[180:183], v163 offset:2048
	ds_read_b128 v[184:187], v163 offset:3072
	s_add_u32 s4, s28, 0x40000
	s_addc_u32 s5, s29, 0
	s_mov_b32 m0, s59
	v_lshl_add_u64 v[240:241], s[4:5], 0, v[140:141]
	ds_read_b128 v[188:191], v162 offset:32768
	ds_read_b128 v[192:195], v162 offset:33792
	ds_read_b128 v[196:199], v162 offset:34816
	ds_read_b128 v[200:203], v162 offset:35840
	ds_read_b128 v[204:207], v162 offset:36864
	ds_read_b128 v[208:211], v162 offset:37888
	ds_read_b128 v[212:215], v162 offset:38912
	ds_read_b128 v[234:237], v162 offset:39936
	global_load_lds_dwordx4 v[240:241], off
	v_lshl_add_u64 v[240:241], s[4:5], 0, v[142:143]
	s_mov_b32 m0, s60
	s_nop 0
	global_load_lds_dwordx4 v[240:241], off
	s_waitcnt vmcnt(8)
	s_waitcnt lgkmcnt(0)
	s_barrier
	s_waitcnt lgkmcnt(0)
	v_mfma_f32_16x16x32_bf16 v[132:135], v[128:131], v[188:191], v[132:135]
	v_mfma_f32_16x16x32_bf16 v[124:127], v[150:153], v[188:191], v[124:127]
	v_mfma_f32_16x16x32_bf16 v[112:115], v[128:131], v[196:199], v[112:115]
	v_mfma_f32_16x16x32_bf16 v[108:111], v[150:153], v[196:199], v[108:111]
	v_mfma_f32_16x16x32_bf16 v[96:99], v[128:131], v[204:207], v[96:99]
	v_mfma_f32_16x16x32_bf16 v[92:95], v[150:153], v[204:207], v[92:95]
	v_mfma_f32_16x16x32_bf16 v[78:81], v[128:131], v[212:215], v[78:81]
	v_mfma_f32_16x16x32_bf16 v[74:77], v[150:153], v[212:215], v[74:77]
	v_mfma_f32_16x16x32_bf16 v[132:135], v[136:139], v[192:195], v[132:135]
	v_mfma_f32_16x16x32_bf16 v[124:127], v[154:157], v[192:195], v[124:127]
	v_mfma_f32_16x16x32_bf16 v[112:115], v[136:139], v[200:203], v[112:115]
	v_mfma_f32_16x16x32_bf16 v[108:111], v[154:157], v[200:203], v[108:111]
	v_mfma_f32_16x16x32_bf16 v[96:99], v[136:139], v[208:211], v[96:99]
	v_mfma_f32_16x16x32_bf16 v[92:95], v[154:157], v[208:211], v[92:95]
	v_mfma_f32_16x16x32_bf16 v[78:81], v[136:139], v[234:237], v[78:81]
	v_mfma_f32_16x16x32_bf16 v[74:77], v[154:157], v[234:237], v[74:77]
	v_mfma_f32_16x16x32_bf16 v[120:123], v[172:175], v[188:191], v[120:123]
	v_mfma_f32_16x16x32_bf16 v[116:119], v[180:183], v[188:191], v[116:119]
	v_mfma_f32_16x16x32_bf16 v[104:107], v[172:175], v[196:199], v[104:107]
	v_mfma_f32_16x16x32_bf16 v[100:103], v[180:183], v[196:199], v[100:103]
	v_mfma_f32_16x16x32_bf16 v[86:89], v[172:175], v[204:207], v[86:89]
	v_mfma_f32_16x16x32_bf16 v[82:85], v[180:183], v[204:207], v[82:85]
	v_mfma_f32_16x16x32_bf16 v[70:73], v[172:175], v[212:215], v[70:73]
	v_mfma_f32_16x16x32_bf16 v[66:69], v[180:183], v[212:215], v[66:69]
	v_mfma_f32_16x16x32_bf16 v[120:123], v[176:179], v[192:195], v[120:123]
	v_mfma_f32_16x16x32_bf16 v[116:119], v[184:187], v[192:195], v[116:119]
	v_mfma_f32_16x16x32_bf16 v[104:107], v[176:179], v[200:203], v[104:107]
	v_mfma_f32_16x16x32_bf16 v[100:103], v[184:187], v[200:203], v[100:103]
	v_mfma_f32_16x16x32_bf16 v[86:89], v[176:179], v[208:211], v[86:89]
	v_mfma_f32_16x16x32_bf16 v[82:85], v[184:187], v[208:211], v[82:85]
	v_mfma_f32_16x16x32_bf16 v[70:73], v[176:179], v[234:237], v[70:73]
	v_mfma_f32_16x16x32_bf16 v[66:69], v[184:187], v[234:237], v[66:69]
	s_barrier
; #define PG8_STAGE(bufoff, gbase, voff) do { _Pragma("unroll") for (int _i = 0; _i < 2; ++_i) \
;         __builtin_amdgcn_global_load_lds((const unsigned*)((const char*)(gbase) + (voff)[_i]), (LAS unsigned*)(lds + (bufoff) + ldsw + _i * 8192), 16, 0, 0); } while (0)
; #define PG8_LDA(dst, b, h) do { _Pragma("unroll") for (int m = 0; m < 4; ++m) _Pragma("unroll") for (int k = 0; k < 2; ++k) dst[m][k] = *(const LAS bf16x8*)(lds + PG8_SA(b, h) + aoff + m * 2048 + k * 1024); } while (0)
; #define PG8_MMA(ai, bj, At, Bt) do { __builtin_amdgcn_s_setprio(1); _Pragma("unroll") for (int m = 0; m < 4; ++m) _Pragma("unroll") for (int n = 0; n < 2; ++n) _Pragma("unroll") for (int k = 0; k < 2; ++k) \
;         acc[ai][bj][m][n] = __builtin_amdgcn_mfma_f32_16x16x32_bf16(Bt[n][k], At[m][k], acc[ai][bj][m][n], 0, 0, 0); __builtin_amdgcn_s_setprio(0); } while (0)
; #define PG8_WAIT_V(n) asm volatile("s_waitcnt vmcnt(" #n ")" ::: "memory")
; #define PG8_WAIT_L(n) asm volatile("s_waitcnt lgkmcnt(" #n ")" ::: "memory")
; #define PG8_BAR __builtin_amdgcn_s_barrier()
; #define PG8_SCHED __builtin_amdgcn_sched_barrier(0)
; template <class Epi, class Sched, bool ALIGN_EPI = true, bool SP2 = true>
; __device__ __forceinline__ void gemm_phase(LAS unsigned char* lds, const Dims g, const Sched& S, const Epi& E) {
;     ...
;             PG8_LDA(At, 1, 1); PG8_STAGE(PG8_SB(1, 0), b3, voffB); PG8_STAGE(PG8_SB(1, 1), b3 + hstepB, voffB); PG8_STAGE(PG8_SA(1, 0), a3, voffA);
;             PG8_WAIT_V(8); PG8_WAIT_L(0); PG8_BAR; PG8_MMA(1, 0, At, B0); PG8_MMA(1, 1, At, B1); PG8_BAR; PG8_SCHED;
;     ...
;         if constexpr (ALIGN_EPI) { if (wr == 0) PG8_BAR; }
	s_add_i32 s4, s33, s37
	v_lshl_add_u64 v[164:165], v[164:165], 0, s[16:17]
	s_mov_b32 m0, s4
	ds_read_b128 v[188:191], v162 offset:49152
	ds_read_b128 v[192:195], v162 offset:50176
	ds_read_b128 v[196:199], v162 offset:51200
	ds_read_b128 v[200:203], v162 offset:52224
	ds_read_b128 v[204:207], v162 offset:53248
	ds_read_b128 v[208:211], v162 offset:54272
	ds_read_b128 v[212:215], v162 offset:55296
	ds_read_b128 v[234:237], v162 offset:56320
	global_load_lds_dwordx4 v[164:165], off
	s_add_i32 m0, s4, 0x2000
	s_add_u32 s4, s26, 0x40080
	v_lshl_add_u64 v[164:165], v[166:167], 0, s[16:17]
	s_addc_u32 s5, s27, 0
	s_add_i32 s26, s51, s37
	global_load_lds_dwordx4 v[164:165], off
	v_lshl_add_u64 v[164:165], s[4:5], 0, v[90:91]
	s_mov_b32 m0, s26
	s_nop 0
	global_load_lds_dwordx4 v[164:165], off
	v_lshl_add_u64 v[164:165], s[4:5], 0, v[144:145]
	s_add_i32 m0, s26, 0x2000
	s_nop 0
	global_load_lds_dwordx4 v[164:165], off
	v_lshl_add_u64 v[164:165], v[216:217], 0, s[16:17]
	s_mov_b32 m0, s61
	s_nop 0
	global_load_lds_dwordx4 v[164:165], off
	v_lshl_add_u64 v[164:165], v[238:239], 0, s[16:17]
	s_mov_b32 m0, s62
	s_nop 0
	global_load_lds_dwordx4 v[164:165], off
	s_waitcnt vmcnt(8)
	s_waitcnt lgkmcnt(0)
	s_barrier
	s_waitcnt lgkmcnt(0)
	v_mfma_f32_16x16x32_bf16 v[62:65], v[128:131], v[188:191], v[62:65]
	v_mfma_f32_16x16x32_bf16 v[58:61], v[150:153], v[188:191], v[58:61]
	v_mfma_f32_16x16x32_bf16 v[46:49], v[128:131], v[196:199], v[46:49]
	v_mfma_f32_16x16x32_bf16 v[42:45], v[150:153], v[196:199], v[42:45]
	v_mfma_f32_16x16x32_bf16 v[30:33], v[128:131], v[204:207], v[30:33]
	v_mfma_f32_16x16x32_bf16 v[26:29], v[150:153], v[204:207], v[26:29]
	v_mfma_f32_16x16x32_bf16 v[14:17], v[128:131], v[212:215], v[14:17]
	v_mfma_f32_16x16x32_bf16 v[10:13], v[150:153], v[212:215], v[10:13]
	v_mfma_f32_16x16x32_bf16 v[62:65], v[136:139], v[192:195], v[62:65]
	v_mfma_f32_16x16x32_bf16 v[58:61], v[154:157], v[192:195], v[58:61]
	v_mfma_f32_16x16x32_bf16 v[46:49], v[136:139], v[200:203], v[46:49]
	v_mfma_f32_16x16x32_bf16 v[42:45], v[154:157], v[200:203], v[42:45]
	v_mfma_f32_16x16x32_bf16 v[30:33], v[136:139], v[208:211], v[30:33]
	v_mfma_f32_16x16x32_bf16 v[26:29], v[154:157], v[208:211], v[26:29]
	v_mfma_f32_16x16x32_bf16 v[14:17], v[136:139], v[234:237], v[14:17]
	v_mfma_f32_16x16x32_bf16 v[10:13], v[154:157], v[234:237], v[10:13]
	v_mfma_f32_16x16x32_bf16 v[54:57], v[172:175], v[188:191], v[54:57]
	v_mfma_f32_16x16x32_bf16 v[50:53], v[180:183], v[188:191], v[50:53]
	v_mfma_f32_16x16x32_bf16 v[38:41], v[172:175], v[196:199], v[38:41]
	v_mfma_f32_16x16x32_bf16 v[34:37], v[180:183], v[196:199], v[34:37]
	v_mfma_f32_16x16x32_bf16 v[22:25], v[172:175], v[204:207], v[22:25]
	v_mfma_f32_16x16x32_bf16 v[18:21], v[180:183], v[204:207], v[18:21]
	v_mfma_f32_16x16x32_bf16 v[6:9], v[172:175], v[212:215], v[6:9]
	v_mfma_f32_16x16x32_bf16 v[2:5], v[180:183], v[212:215], v[2:5]
	v_mfma_f32_16x16x32_bf16 v[54:57], v[176:179], v[192:195], v[54:57]
	v_mfma_f32_16x16x32_bf16 v[50:53], v[184:187], v[192:195], v[50:53]
	v_mfma_f32_16x16x32_bf16 v[38:41], v[176:179], v[200:203], v[38:41]
	v_mfma_f32_16x16x32_bf16 v[34:37], v[184:187], v[200:203], v[34:37]
	v_mfma_f32_16x16x32_bf16 v[22:25], v[176:179], v[208:211], v[22:25]
	v_mfma_f32_16x16x32_bf16 v[18:21], v[184:187], v[208:211], v[18:21]
	v_mfma_f32_16x16x32_bf16 v[6:9], v[176:179], v[234:237], v[6:9]
	v_mfma_f32_16x16x32_bf16 v[2:5], v[184:187], v[234:237], v[2:5]
	s_barrier
	s_add_i32 s3, s3, 2
	s_add_u32 s24, s24, 0x100
	s_addc_u32 s25, s25, 0
	s_add_u32 s1, s1, 0x100
	s_addc_u32 s2, s2, 0
	s_cmp_gt_u32 s3, 13
	s_cbranch_scc0 .LBB0_1402
	s_and_b64 vcc, exec, s[48:49]
	s_cbranch_vccz .LBB0_1405
	s_barrier

; #define PG8_STAGE(bufoff, gbase, voff) do { _Pragma("unroll") for (int _i = 0; _i < 2; ++_i) \
;         __builtin_amdgcn_global_load_lds((const unsigned*)((const char*)(gbase) + (voff)[_i]), (LAS unsigned*)(lds + (bufoff) + ldsw + _i * 8192), 16, 0, 0); } while (0)
; #define PG8_LDA(dst, b, h) do { _Pragma("unroll") for (int m = 0; m < 4; ++m) _Pragma("unroll") for (int k = 0; k < 2; ++k) dst[m][k] = *(const LAS bf16x8*)(lds + PG8_SA(b, h) + aoff + m * 2048 + k * 1024); } while (0)
; #define PG8_LDB(dst, b, h) do { _Pragma("unroll") for (int n = 0; n < 2; ++n) _Pragma("unroll") for (int k = 0; k < 2; ++k) dst[n][k] = *(const LAS bf16x8*)(lds + PG8_SB(b, h) + boff + n * 2048 + k * 1024); } while (0)
; #define PG8_WAIT_V(n) asm volatile("s_waitcnt vmcnt(" #n ")" ::: "memory")
; #define PG8_WAIT_L(n) asm volatile("s_waitcnt lgkmcnt(" #n ")" ::: "memory")
; #define PG8_BAR __builtin_amdgcn_s_barrier()
; template <class Epi, class Sched, bool ALIGN_EPI = true, bool SP2 = true>
; __device__ __forceinline__ void gemm_phase(LAS unsigned char* lds, const Dims g, const Sched& S, const Epi& E) {
;     ...
;         const bool has_next = S.next(ui + 1, nxt);
;         const char* nA = has_next ? nxt.A : cA; const char* nB = has_next ? nxt.B : cB;
;         for (int t = 0; t < nt; t += 2) {
;             const bool last = (t == nt - 2);
;             const char* a1 = cA + (size_t)(t + 1) * kstep;
;             const char* a2 = last ? nA : cA + (size_t)(t + 2) * kstep; const char* b2 = last ? nB : cB + (size_t)(t + 2) * kstep;
;             const char* a3 = a2 + kstep; const char* b3 = b2 + kstep;
;             if constexpr (SP2) {
;             PG8_LDB(B0, 0, 0); PG8_LDB(B1, 0, 1); PG8_SCHED; PG8_LDA(At, 0, 0); PG8_STAGE(PG8_SA(1, 1), a1 + hstepA, voffA);
;             PG8_WAIT_V(8); PG8_WAIT_L(0); PG8_BAR; PG8_MMA(0, 0, At, B0); PG8_MMA(0, 1, At, B1); PG8_BAR; PG8_SCHED;
;             PG8_LDA(At, 0, 1); PG8_STAGE(PG8_SB(0, 0), b2, voffB); PG8_STAGE(PG8_SB(0, 1), b2 + hstepB, voffB); PG8_STAGE(PG8_SA(0, 0), a2, voffA);
;             PG8_WAIT_V(8); PG8_WAIT_L(0); PG8_BAR; PG8_MMA(1, 0, At, B0); PG8_MMA(1, 1, At, B1); PG8_BAR; PG8_SCHED;
;             PG8_LDB(B0, 1, 0); PG8_LDB(B1, 1, 1); PG8_SCHED; PG8_LDA(At, 1, 0); PG8_STAGE(PG8_SA(0, 1), a2 + hstepA, voffA);
;             PG8_WAIT_V(8); PG8_WAIT_L(0); PG8_BAR; PG8_MMA(0, 0, At, B0); PG8_MMA(0, 1, At, B1); PG8_BAR; PG8_SCHED;
.LBB0_1429:
	s_add_u32 s4, s24, 0xfffc0080
	s_addc_u32 s5, s25, -1
	s_add_i32 s33, 0, 0x10000
	s_cmp_eq_u32 s3, 12
	s_cselect_b32 s29, s57, s5
	s_cselect_b32 s28, s56, s4
	s_cselect_b32 s27, s59, s2
	s_cselect_b32 s26, s58, s1
	s_add_i32 s53, 0, 0x14000
	v_add_u32_e32 v144, s33, v178
	v_add_u32_e32 v162, s53, v178
	ds_read_b128 v[128:131], v144
	ds_read_b128 v[132:135], v144 offset:1024
	ds_read_b128 v[140:143], v144 offset:2048
	ds_read_b128 v[144:147], v144 offset:3072
	ds_read_b128 v[158:161], v162
	ds_read_b128 v[172:175], v162 offset:1024
	ds_read_b128 v[182:185], v162 offset:2048
	ds_read_b128 v[186:189], v162 offset:3072
	v_lshl_add_u64 v[162:163], s[24:25], 0, v[154:155]
	s_add_i32 m0, s13, 0xc000
	ds_read_b128 v[190:193], v180
	ds_read_b128 v[194:197], v180 offset:1024
	ds_read_b128 v[198:201], v180 offset:2048
	ds_read_b128 v[202:205], v180 offset:3072
	ds_read_b128 v[206:209], v180 offset:4096
	ds_read_b128 v[210:213], v180 offset:5120
	ds_read_b128 v[214:217], v180 offset:6144
	ds_read_b128 v[234:237], v180 offset:7168
	global_load_lds_dwordx4 v[162:163], off
	v_lshl_add_u64 v[162:163], s[24:25], 0, v[156:157]
	s_add_i32 m0, s13, 0xe000
	s_nop 0
	global_load_lds_dwordx4 v[162:163], off
	s_waitcnt vmcnt(8)
	s_waitcnt lgkmcnt(0)
	s_barrier
	s_waitcnt lgkmcnt(0)
	v_mfma_f32_16x16x32_bf16 v[136:139], v[128:131], v[190:193], v[136:139]
	v_mfma_f32_16x16x32_bf16 v[124:127], v[140:143], v[190:193], v[124:127]
	v_mfma_f32_16x16x32_bf16 v[112:115], v[128:131], v[198:201], v[112:115]
	v_mfma_f32_16x16x32_bf16 v[108:111], v[140:143], v[198:201], v[108:111]
	v_mfma_f32_16x16x32_bf16 v[96:99], v[128:131], v[206:209], v[96:99]
	v_mfma_f32_16x16x32_bf16 v[92:95], v[140:143], v[206:209], v[92:95]
	v_mfma_f32_16x16x32_bf16 v[78:81], v[128:131], v[214:217], v[78:81]
	v_mfma_f32_16x16x32_bf16 v[74:77], v[140:143], v[214:217], v[74:77]
	v_mfma_f32_16x16x32_bf16 v[136:139], v[132:135], v[194:197], v[136:139]
	v_mfma_f32_16x16x32_bf16 v[124:127], v[144:147], v[194:197], v[124:127]
	v_mfma_f32_16x16x32_bf16 v[112:115], v[132:135], v[202:205], v[112:115]
	v_mfma_f32_16x16x32_bf16 v[108:111], v[144:147], v[202:205], v[108:111]
	v_mfma_f32_16x16x32_bf16 v[96:99], v[132:135], v[210:213], v[96:99]
	v_mfma_f32_16x16x32_bf16 v[92:95], v[144:147], v[210:213], v[92:95]
	v_mfma_f32_16x16x32_bf16 v[78:81], v[132:135], v[234:237], v[78:81]
	v_mfma_f32_16x16x32_bf16 v[74:77], v[144:147], v[234:237], v[74:77]
	v_mfma_f32_16x16x32_bf16 v[120:123], v[158:161], v[190:193], v[120:123]
	v_mfma_f32_16x16x32_bf16 v[116:119], v[182:185], v[190:193], v[116:119]
	v_mfma_f32_16x16x32_bf16 v[104:107], v[158:161], v[198:201], v[104:107]
	v_mfma_f32_16x16x32_bf16 v[100:103], v[182:185], v[198:201], v[100:103]
	v_mfma_f32_16x16x32_bf16 v[86:89], v[158:161], v[206:209], v[86:89]
	v_mfma_f32_16x16x32_bf16 v[82:85], v[182:185], v[206:209], v[82:85]
	v_mfma_f32_16x16x32_bf16 v[70:73], v[158:161], v[214:217], v[70:73]
	v_mfma_f32_16x16x32_bf16 v[66:69], v[182:185], v[214:217], v[66:69]
	v_mfma_f32_16x16x32_bf16 v[120:123], v[172:175], v[194:197], v[120:123]
	v_mfma_f32_16x16x32_bf16 v[116:119], v[186:189], v[194:197], v[116:119]
	v_mfma_f32_16x16x32_bf16 v[104:107], v[172:175], v[202:205], v[104:107]
	v_mfma_f32_16x16x32_bf16 v[100:103], v[186:189], v[202:205], v[100:103]
	v_mfma_f32_16x16x32_bf16 v[86:89], v[172:175], v[210:213], v[86:89]
	v_mfma_f32_16x16x32_bf16 v[82:85], v[186:189], v[210:213], v[82:85]
	v_mfma_f32_16x16x32_bf16 v[70:73], v[172:175], v[234:237], v[70:73]
	v_mfma_f32_16x16x32_bf16 v[66:69], v[186:189], v[234:237], v[66:69]
	s_barrier
	s_add_i32 s4, s33, s30
	v_lshl_add_u64 v[162:163], s[26:27], 0, v[90:91]
	s_mov_b32 m0, s4
	ds_read_b128 v[190:193], v180 offset:16384
	ds_read_b128 v[194:197], v180 offset:17408
	ds_read_b128 v[198:201], v180 offset:18432
	ds_read_b128 v[202:205], v180 offset:19456
	ds_read_b128 v[206:209], v180 offset:20480
	ds_read_b128 v[210:213], v180 offset:21504
	ds_read_b128 v[214:217], v180 offset:22528
	ds_read_b128 v[234:237], v180 offset:23552
	global_load_lds_dwordx4 v[162:163], off
	s_add_i32 m0, s4, 0x2000
	s_add_u32 s4, s26, 0x40000
	v_lshl_add_u64 v[164:165], s[26:27], 0, v[152:153]
	s_addc_u32 s5, s27, 0
	s_add_i32 s33, s53, s30
	global_load_lds_dwordx4 v[164:165], off
	v_lshl_add_u64 v[166:167], s[4:5], 0, v[90:91]
	s_mov_b32 m0, s33
	v_lshl_add_u64 v[238:239], s[28:29], 0, v[150:151]
	global_load_lds_dwordx4 v[166:167], off
	v_lshl_add_u64 v[166:167], s[4:5], 0, v[152:153]
	s_add_i32 m0, s33, 0x2000
	s_nop 0
	global_load_lds_dwordx4 v[166:167], off
	v_lshl_add_u64 v[166:167], s[28:29], 0, v[148:149]
	s_mov_b32 m0, s13
	s_nop 0
	global_load_lds_dwordx4 v[166:167], off
	s_mov_b32 m0, s36
	s_nop 0
	global_load_lds_dwordx4 v[238:239], off
	s_waitcnt vmcnt(8)
	s_waitcnt lgkmcnt(0)
	s_barrier
; #define PG8_STAGE(bufoff, gbase, voff) do { _Pragma("unroll") for (int _i = 0; _i < 2; ++_i) \
;         __builtin_amdgcn_global_load_lds((const unsigned*)((const char*)(gbase) + (voff)[_i]), (LAS unsigned*)(lds + (bufoff) + ldsw + _i * 8192), 16, 0, 0); } while (0)
; #define PG8_LDA(dst, b, h) do { _Pragma("unroll") for (int m = 0; m < 4; ++m) _Pragma("unroll") for (int k = 0; k < 2; ++k) dst[m][k] = *(const LAS bf16x8*)(lds + PG8_SA(b, h) + aoff + m * 2048 + k * 1024); } while (0)
; #define PG8_LDB(dst, b, h) do { _Pragma("unroll") for (int n = 0; n < 2; ++n) _Pragma("unroll") for (int k = 0; k < 2; ++k) dst[n][k] = *(const LAS bf16x8*)(lds + PG8_SB(b, h) + boff + n * 2048 + k * 1024); } while (0)
; #define PG8_MMA(ai, bj, At, Bt) do { __builtin_amdgcn_s_setprio(1); _Pragma("unroll") for (int m = 0; m < 4; ++m) _Pragma("unroll") for (int n = 0; n < 2; ++n) _Pragma("unroll") for (int k = 0; k < 2; ++k) \
;         acc[ai][bj][m][n] = __builtin_amdgcn_mfma_f32_16x16x32_bf16(Bt[n][k], At[m][k], acc[ai][bj][m][n], 0, 0, 0); __builtin_amdgcn_s_setprio(0); } while (0)
; #define PG8_WAIT_V(n) asm volatile("s_waitcnt vmcnt(" #n ")" ::: "memory")
; #define PG8_WAIT_L(n) asm volatile("s_waitcnt lgkmcnt(" #n ")" ::: "memory")
; #define PG8_BAR __builtin_amdgcn_s_barrier()
; #define PG8_SCHED __builtin_amdgcn_sched_barrier(0)
; template <class Epi, class Sched, bool ALIGN_EPI = true, bool SP2 = true>
; __device__ __forceinline__ void gemm_phase(LAS unsigned char* lds, const Dims g, const Sched& S, const Epi& E) {
;     ...
;             PG8_WAIT_V(8); PG8_WAIT_L(0); PG8_BAR; PG8_MMA(1, 0, At, B0); PG8_MMA(1, 1, At, B1); PG8_BAR; PG8_SCHED;
;             PG8_LDB(B0, 1, 0); PG8_LDB(B1, 1, 1); PG8_SCHED; PG8_LDA(At, 1, 0); PG8_STAGE(PG8_SA(0, 1), a2 + hstepA, voffA);
;             PG8_WAIT_V(8); PG8_WAIT_L(0); PG8_BAR; PG8_MMA(0, 0, At, B0); PG8_MMA(0, 1, At, B1); PG8_BAR; PG8_SCHED;
;             PG8_LDA(At, 1, 1); PG8_STAGE(PG8_SB(1, 0), b3, voffB); PG8_STAGE(PG8_SB(1, 1), b3 + hstepB, voffB); PG8_STAGE(PG8_SA(1, 0), a3, voffA);
	s_waitcnt lgkmcnt(0)
	v_mfma_f32_16x16x32_bf16 v[62:65], v[128:131], v[190:193], v[62:65]
	v_mfma_f32_16x16x32_bf16 v[58:61], v[140:143], v[190:193], v[58:61]
	v_mfma_f32_16x16x32_bf16 v[46:49], v[128:131], v[198:201], v[46:49]
	v_mfma_f32_16x16x32_bf16 v[42:45], v[140:143], v[198:201], v[42:45]
	v_mfma_f32_16x16x32_bf16 v[30:33], v[128:131], v[206:209], v[30:33]
	v_mfma_f32_16x16x32_bf16 v[26:29], v[140:143], v[206:209], v[26:29]
	v_mfma_f32_16x16x32_bf16 v[14:17], v[128:131], v[214:217], v[14:17]
	v_mfma_f32_16x16x32_bf16 v[10:13], v[140:143], v[214:217], v[10:13]
	v_mfma_f32_16x16x32_bf16 v[62:65], v[132:135], v[194:197], v[62:65]
	v_mfma_f32_16x16x32_bf16 v[58:61], v[144:147], v[194:197], v[58:61]
	v_mfma_f32_16x16x32_bf16 v[46:49], v[132:135], v[202:205], v[46:49]
	v_mfma_f32_16x16x32_bf16 v[42:45], v[144:147], v[202:205], v[42:45]
	v_mfma_f32_16x16x32_bf16 v[30:33], v[132:135], v[210:213], v[30:33]
	v_mfma_f32_16x16x32_bf16 v[26:29], v[144:147], v[210:213], v[26:29]
	v_mfma_f32_16x16x32_bf16 v[14:17], v[132:135], v[234:237], v[14:17]
	v_mfma_f32_16x16x32_bf16 v[10:13], v[144:147], v[234:237], v[10:13]
	v_mfma_f32_16x16x32_bf16 v[54:57], v[158:161], v[190:193], v[54:57]
	v_mfma_f32_16x16x32_bf16 v[50:53], v[182:185], v[190:193], v[50:53]
	v_mfma_f32_16x16x32_bf16 v[38:41], v[158:161], v[198:201], v[38:41]
	v_mfma_f32_16x16x32_bf16 v[34:37], v[182:185], v[198:201], v[34:37]
	v_mfma_f32_16x16x32_bf16 v[22:25], v[158:161], v[206:209], v[22:25]
	v_mfma_f32_16x16x32_bf16 v[18:21], v[182:185], v[206:209], v[18:21]
	v_mfma_f32_16x16x32_bf16 v[6:9], v[158:161], v[214:217], v[6:9]
	v_mfma_f32_16x16x32_bf16 v[2:5], v[182:185], v[214:217], v[2:5]
	v_mfma_f32_16x16x32_bf16 v[54:57], v[172:175], v[194:197], v[54:57]
	v_mfma_f32_16x16x32_bf16 v[50:53], v[186:189], v[194:197], v[50:53]
	v_mfma_f32_16x16x32_bf16 v[38:41], v[172:175], v[202:205], v[38:41]
	v_mfma_f32_16x16x32_bf16 v[34:37], v[186:189], v[202:205], v[34:37]
	v_mfma_f32_16x16x32_bf16 v[22:25], v[172:175], v[210:213], v[22:25]
	v_mfma_f32_16x16x32_bf16 v[18:21], v[186:189], v[210:213], v[18:21]
	v_mfma_f32_16x16x32_bf16 v[6:9], v[172:175], v[234:237], v[6:9]
	v_mfma_f32_16x16x32_bf16 v[2:5], v[186:189], v[234:237], v[2:5]
	s_barrier
	s_add_i32 s33, 0, 0x18000
	s_add_i32 s53, 0, 0x1c000
	v_add_u32_e32 v144, s33, v178
	v_add_u32_e32 v181, s53, v178
	ds_read_b128 v[128:131], v144
	ds_read_b128 v[132:135], v144 offset:1024
	ds_read_b128 v[140:143], v144 offset:2048
	ds_read_b128 v[144:147], v144 offset:3072
	ds_read_b128 v[158:161], v181
	ds_read_b128 v[172:175], v181 offset:1024
	ds_read_b128 v[182:185], v181 offset:2048
	ds_read_b128 v[186:189], v181 offset:3072
	s_add_u32 s4, s28, 0x40000
	s_addc_u32 s5, s29, 0
	s_mov_b32 m0, s37
	v_lshl_add_u64 v[240:241], s[4:5], 0, v[148:149]
	ds_read_b128 v[190:193], v180 offset:32768
	ds_read_b128 v[194:197], v180 offset:33792
	ds_read_b128 v[198:201], v180 offset:34816
	ds_read_b128 v[202:205], v180 offset:35840
	ds_read_b128 v[206:209], v180 offset:36864
	ds_read_b128 v[210:213], v180 offset:37888
	ds_read_b128 v[214:217], v180 offset:38912
	ds_read_b128 v[234:237], v180 offset:39936
	global_load_lds_dwordx4 v[240:241], off
	v_lshl_add_u64 v[240:241], s[4:5], 0, v[150:151]
	s_mov_b32 m0, s60
	s_nop 0
	global_load_lds_dwordx4 v[240:241], off
	s_waitcnt vmcnt(8)
	s_waitcnt lgkmcnt(0)
	s_barrier
	s_waitcnt lgkmcnt(0)
	v_mfma_f32_16x16x32_bf16 v[136:139], v[128:131], v[190:193], v[136:139]
	v_mfma_f32_16x16x32_bf16 v[124:127], v[140:143], v[190:193], v[124:127]
	v_mfma_f32_16x16x32_bf16 v[112:115], v[128:131], v[198:201], v[112:115]
	v_mfma_f32_16x16x32_bf16 v[108:111], v[140:143], v[198:201], v[108:111]
	v_mfma_f32_16x16x32_bf16 v[96:99], v[128:131], v[206:209], v[96:99]
	v_mfma_f32_16x16x32_bf16 v[92:95], v[140:143], v[206:209], v[92:95]
	v_mfma_f32_16x16x32_bf16 v[78:81], v[128:131], v[214:217], v[78:81]
	v_mfma_f32_16x16x32_bf16 v[74:77], v[140:143], v[214:217], v[74:77]
	v_mfma_f32_16x16x32_bf16 v[136:139], v[132:135], v[194:197], v[136:139]
	v_mfma_f32_16x16x32_bf16 v[124:127], v[144:147], v[194:197], v[124:127]
	v_mfma_f32_16x16x32_bf16 v[112:115], v[132:135], v[202:205], v[112:115]
	v_mfma_f32_16x16x32_bf16 v[108:111], v[144:147], v[202:205], v[108:111]
	v_mfma_f32_16x16x32_bf16 v[96:99], v[132:135], v[210:213], v[96:99]
	v_mfma_f32_16x16x32_bf16 v[92:95], v[144:147], v[210:213], v[92:95]
	v_mfma_f32_16x16x32_bf16 v[78:81], v[132:135], v[234:237], v[78:81]
	v_mfma_f32_16x16x32_bf16 v[74:77], v[144:147], v[234:237], v[74:77]
	v_mfma_f32_16x16x32_bf16 v[120:123], v[158:161], v[190:193], v[120:123]
	v_mfma_f32_16x16x32_bf16 v[116:119], v[182:185], v[190:193], v[116:119]
	v_mfma_f32_16x16x32_bf16 v[104:107], v[158:161], v[198:201], v[104:107]
	v_mfma_f32_16x16x32_bf16 v[100:103], v[182:185], v[198:201], v[100:103]
	v_mfma_f32_16x16x32_bf16 v[86:89], v[158:161], v[206:209], v[86:89]
	v_mfma_f32_16x16x32_bf16 v[82:85], v[182:185], v[206:209], v[82:85]
	v_mfma_f32_16x16x32_bf16 v[70:73], v[158:161], v[214:217], v[70:73]
	v_mfma_f32_16x16x32_bf16 v[66:69], v[182:185], v[214:217], v[66:69]
	v_mfma_f32_16x16x32_bf16 v[120:123], v[172:175], v[194:197], v[120:123]
	v_mfma_f32_16x16x32_bf16 v[116:119], v[186:189], v[194:197], v[116:119]
	v_mfma_f32_16x16x32_bf16 v[104:107], v[172:175], v[202:205], v[104:107]
	v_mfma_f32_16x16x32_bf16 v[100:103], v[186:189], v[202:205], v[100:103]
	v_mfma_f32_16x16x32_bf16 v[86:89], v[172:175], v[210:213], v[86:89]
	v_mfma_f32_16x16x32_bf16 v[82:85], v[186:189], v[210:213], v[82:85]
	v_mfma_f32_16x16x32_bf16 v[70:73], v[172:175], v[234:237], v[70:73]
	v_mfma_f32_16x16x32_bf16 v[66:69], v[186:189], v[234:237], v[66:69]
	s_barrier
; #define PG8_STAGE(bufoff, gbase, voff) do { _Pragma("unroll") for (int _i = 0; _i < 2; ++_i) \
;         __builtin_amdgcn_global_load_lds((const unsigned*)((const char*)(gbase) + (voff)[_i]), (LAS unsigned*)(lds + (bufoff) + ldsw + _i * 8192), 16, 0, 0); } while (0)
; #define PG8_LDA(dst, b, h) do { _Pragma("unroll") for (int m = 0; m < 4; ++m) _Pragma("unroll") for (int k = 0; k < 2; ++k) dst[m][k] = *(const LAS bf16x8*)(lds + PG8_SA(b, h) + aoff + m * 2048 + k * 1024); } while (0)
; #define PG8_MMA(ai, bj, At, Bt) do { __builtin_amdgcn_s_setprio(1); _Pragma("unroll") for (int m = 0; m < 4; ++m) _Pragma("unroll") for (int n = 0; n < 2; ++n) _Pragma("unroll") for (int k = 0; k < 2; ++k) \
;         acc[ai][bj][m][n] = __builtin_amdgcn_mfma_f32_16x16x32_bf16(Bt[n][k], At[m][k], acc[ai][bj][m][n], 0, 0, 0); __builtin_amdgcn_s_setprio(0); } while (0)
; #define PG8_WAIT_V(n) asm volatile("s_waitcnt vmcnt(" #n ")" ::: "memory")
; #define PG8_WAIT_L(n) asm volatile("s_waitcnt lgkmcnt(" #n ")" ::: "memory")
; #define PG8_BAR __builtin_amdgcn_s_barrier()
; #define PG8_SCHED __builtin_amdgcn_sched_barrier(0)
; template <class Epi, class Sched, bool ALIGN_EPI = true, bool SP2 = true>
; __device__ __forceinline__ void gemm_phase(LAS unsigned char* lds, const Dims g, const Sched& S, const Epi& E) {
;     ...
;             PG8_LDA(At, 1, 1); PG8_STAGE(PG8_SB(1, 0), b3, voffB); PG8_STAGE(PG8_SB(1, 1), b3 + hstepB, voffB); PG8_STAGE(PG8_SA(1, 0), a3, voffA);
;             PG8_WAIT_V(8); PG8_WAIT_L(0); PG8_BAR; PG8_MMA(1, 0, At, B0); PG8_MMA(1, 1, At, B1); PG8_BAR; PG8_SCHED;
;     ...
;         if constexpr (ALIGN_EPI) { if (wr == 0) PG8_BAR; }
	s_add_i32 s4, s33, s30
	v_lshl_add_u64 v[162:163], v[162:163], 0, s[16:17]
	s_mov_b32 m0, s4
	ds_read_b128 v[190:193], v180 offset:49152
	ds_read_b128 v[194:197], v180 offset:50176
	ds_read_b128 v[198:201], v180 offset:51200
	ds_read_b128 v[202:205], v180 offset:52224
	ds_read_b128 v[206:209], v180 offset:53248
	ds_read_b128 v[210:213], v180 offset:54272
	ds_read_b128 v[214:217], v180 offset:55296
	ds_read_b128 v[234:237], v180 offset:56320
	global_load_lds_dwordx4 v[162:163], off
	s_add_i32 m0, s4, 0x2000
	s_add_u32 s4, s26, 0x40080
	v_lshl_add_u64 v[162:163], v[164:165], 0, s[16:17]
	s_addc_u32 s5, s27, 0
	s_add_i32 s26, s53, s30
	global_load_lds_dwordx4 v[162:163], off
	v_lshl_add_u64 v[162:163], s[4:5], 0, v[90:91]
	s_mov_b32 m0, s26
	s_nop 0
	global_load_lds_dwordx4 v[162:163], off
	v_lshl_add_u64 v[162:163], s[4:5], 0, v[152:153]
	s_add_i32 m0, s26, 0x2000
	s_nop 0
	global_load_lds_dwordx4 v[162:163], off
	v_lshl_add_u64 v[162:163], v[166:167], 0, s[16:17]
	s_mov_b32 m0, s61
	s_nop 0
	global_load_lds_dwordx4 v[162:163], off
	v_lshl_add_u64 v[162:163], v[238:239], 0, s[16:17]
	s_mov_b32 m0, s62
	s_nop 0
	global_load_lds_dwordx4 v[162:163], off
	s_waitcnt vmcnt(8)
	s_waitcnt lgkmcnt(0)
	s_barrier
	s_waitcnt lgkmcnt(0)
	v_mfma_f32_16x16x32_bf16 v[62:65], v[128:131], v[190:193], v[62:65]
	v_mfma_f32_16x16x32_bf16 v[58:61], v[140:143], v[190:193], v[58:61]
	v_mfma_f32_16x16x32_bf16 v[46:49], v[128:131], v[198:201], v[46:49]
	v_mfma_f32_16x16x32_bf16 v[42:45], v[140:143], v[198:201], v[42:45]
	v_mfma_f32_16x16x32_bf16 v[30:33], v[128:131], v[206:209], v[30:33]
	v_mfma_f32_16x16x32_bf16 v[26:29], v[140:143], v[206:209], v[26:29]
	v_mfma_f32_16x16x32_bf16 v[14:17], v[128:131], v[214:217], v[14:17]
	v_mfma_f32_16x16x32_bf16 v[10:13], v[140:143], v[214:217], v[10:13]
	v_mfma_f32_16x16x32_bf16 v[62:65], v[132:135], v[194:197], v[62:65]
	v_mfma_f32_16x16x32_bf16 v[58:61], v[144:147], v[194:197], v[58:61]
	v_mfma_f32_16x16x32_bf16 v[46:49], v[132:135], v[202:205], v[46:49]
	v_mfma_f32_16x16x32_bf16 v[42:45], v[144:147], v[202:205], v[42:45]
	v_mfma_f32_16x16x32_bf16 v[30:33], v[132:135], v[210:213], v[30:33]
	v_mfma_f32_16x16x32_bf16 v[26:29], v[144:147], v[210:213], v[26:29]
	v_mfma_f32_16x16x32_bf16 v[14:17], v[132:135], v[234:237], v[14:17]
	v_mfma_f32_16x16x32_bf16 v[10:13], v[144:147], v[234:237], v[10:13]
	v_mfma_f32_16x16x32_bf16 v[54:57], v[158:161], v[190:193], v[54:57]
	v_mfma_f32_16x16x32_bf16 v[50:53], v[182:185], v[190:193], v[50:53]
	v_mfma_f32_16x16x32_bf16 v[38:41], v[158:161], v[198:201], v[38:41]
	v_mfma_f32_16x16x32_bf16 v[34:37], v[182:185], v[198:201], v[34:37]
	v_mfma_f32_16x16x32_bf16 v[22:25], v[158:161], v[206:209], v[22:25]
	v_mfma_f32_16x16x32_bf16 v[18:21], v[182:185], v[206:209], v[18:21]
	v_mfma_f32_16x16x32_bf16 v[6:9], v[158:161], v[214:217], v[6:9]
	v_mfma_f32_16x16x32_bf16 v[2:5], v[182:185], v[214:217], v[2:5]
	v_mfma_f32_16x16x32_bf16 v[54:57], v[172:175], v[194:197], v[54:57]
	v_mfma_f32_16x16x32_bf16 v[50:53], v[186:189], v[194:197], v[50:53]
	v_mfma_f32_16x16x32_bf16 v[38:41], v[172:175], v[202:205], v[38:41]
	v_mfma_f32_16x16x32_bf16 v[34:37], v[186:189], v[202:205], v[34:37]
	v_mfma_f32_16x16x32_bf16 v[22:25], v[172:175], v[210:213], v[22:25]
	v_mfma_f32_16x16x32_bf16 v[18:21], v[186:189], v[210:213], v[18:21]
	v_mfma_f32_16x16x32_bf16 v[6:9], v[172:175], v[234:237], v[6:9]
	v_mfma_f32_16x16x32_bf16 v[2:5], v[186:189], v[234:237], v[2:5]
	s_barrier
	s_add_i32 s3, s3, 2
	s_add_u32 s24, s24, 0x100
	s_addc_u32 s25, s25, 0
	s_add_u32 s1, s1, 0x100
	s_addc_u32 s2, s2, 0
	s_cmp_gt_u32 s3, 13
	s_cbranch_scc0 .LBB0_1429
	s_and_b64 vcc, exec, s[50:51]
	s_cbranch_vccz .LBB0_1432
	s_barrier

; #define PG8_STAGE(bufoff, gbase, voff) do { _Pragma("unroll") for (int _i = 0; _i < 2; ++_i) \
;         __builtin_amdgcn_global_load_lds((const unsigned*)((const char*)(gbase) + (voff)[_i]), (LAS unsigned*)(lds + (bufoff) + ldsw + _i * 8192), 16, 0, 0); } while (0)
; #define PG8_LDA(dst, b, h) do { _Pragma("unroll") for (int m = 0; m < 4; ++m) _Pragma("unroll") for (int k = 0; k < 2; ++k) dst[m][k] = *(const LAS bf16x8*)(lds + PG8_SA(b, h) + aoff + m * 2048 + k * 1024); } while (0)
; #define PG8_LDB(dst, b, h) do { _Pragma("unroll") for (int n = 0; n < 2; ++n) _Pragma("unroll") for (int k = 0; k < 2; ++k) dst[n][k] = *(const LAS bf16x8*)(lds + PG8_SB(b, h) + boff + n * 2048 + k * 1024); } while (0)
; #define PG8_WAIT_V(n) asm volatile("s_waitcnt vmcnt(" #n ")" ::: "memory")
; #define PG8_WAIT_L(n) asm volatile("s_waitcnt lgkmcnt(" #n ")" ::: "memory")
; #define PG8_BAR __builtin_amdgcn_s_barrier()
; template <class Epi, class Sched, bool ALIGN_EPI = true, bool SP2 = true>
; __device__ __forceinline__ void gemm_phase(LAS unsigned char* lds, const Dims g, const Sched& S, const Epi& E) {
;     ...
;         const bool has_next = S.next(ui + 1, nxt);
;         const char* nA = has_next ? nxt.A : cA; const char* nB = has_next ? nxt.B : cB;
;         for (int t = 0; t < nt; t += 2) {
;             const bool last = (t == nt - 2);
;             const char* a1 = cA + (size_t)(t + 1) * kstep;
;             const char* a2 = last ? nA : cA + (size_t)(t + 2) * kstep; const char* b2 = last ? nB : cB + (size_t)(t + 2) * kstep;
;             const char* a3 = a2 + kstep; const char* b3 = b2 + kstep;
;             if constexpr (SP2) {
;             PG8_LDB(B0, 0, 0); PG8_LDB(B1, 0, 1); PG8_SCHED; PG8_LDA(At, 0, 0); PG8_STAGE(PG8_SA(1, 1), a1 + hstepA, voffA);
;             PG8_WAIT_V(8); PG8_WAIT_L(0); PG8_BAR; PG8_MMA(0, 0, At, B0); PG8_MMA(0, 1, At, B1); PG8_BAR; PG8_SCHED;
;             PG8_LDA(At, 0, 1); PG8_STAGE(PG8_SB(0, 0), b2, voffB); PG8_STAGE(PG8_SB(0, 1), b2 + hstepB, voffB); PG8_STAGE(PG8_SA(0, 0), a2, voffA);
;             PG8_WAIT_V(8); PG8_WAIT_L(0); PG8_BAR; PG8_MMA(1, 0, At, B0); PG8_MMA(1, 1, At, B1); PG8_BAR; PG8_SCHED;
;             PG8_LDB(B0, 1, 0); PG8_LDB(B1, 1, 1); PG8_SCHED; PG8_LDA(At, 1, 0); PG8_STAGE(PG8_SA(0, 1), a2 + hstepA, voffA);
;             PG8_WAIT_V(8); PG8_WAIT_L(0); PG8_BAR; PG8_MMA(0, 0, At, B0); PG8_MMA(0, 1, At, B1); PG8_BAR; PG8_SCHED;
.LBB0_1515:
	s_add_u32 s37, s54, 0xfff80080
	s_addc_u32 s45, s55, -1
	s_add_i32 s70, 0, 0x10000
	s_cmp_eq_u32 s35, 28
	s_cselect_b32 s59, s51, s45
	s_cselect_b32 s58, s50, s37
	v_add_u32_e32 v90, s70, v150
	s_cselect_b32 s57, s53, s3
	s_cselect_b32 s56, s52, s2
	s_add_i32 s37, 0, 0x14000
	ds_read_b128 v[140:143], v90
	ds_read_b128 v[144:147], v90 offset:1024
	ds_read_b128 v[154:157], v90 offset:2048
	ds_read_b128 v[158:161], v90 offset:3072
	v_add_u32_e32 v90, s37, v150
	ds_read_b128 v[172:175], v90
	ds_read_b128 v[176:179], v90 offset:1024
	ds_read_b128 v[180:183], v90 offset:2048
	ds_read_b128 v[184:187], v90 offset:3072
	v_lshl_add_u64 v[162:163], s[54:55], 0, v[136:137]
	s_add_i32 m0, s63, 0xc000
	ds_read_b128 v[188:191], v152
	ds_read_b128 v[192:195], v152 offset:1024
	ds_read_b128 v[196:199], v152 offset:2048
	ds_read_b128 v[200:203], v152 offset:3072
	ds_read_b128 v[204:207], v152 offset:4096
	ds_read_b128 v[208:211], v152 offset:5120
	ds_read_b128 v[212:215], v152 offset:6144
	ds_read_b128 v[234:237], v152 offset:7168
	global_load_lds_dwordx4 v[162:163], off
	v_lshl_add_u64 v[162:163], s[54:55], 0, v[138:139]
	s_add_i32 m0, s63, 0xe000
	s_nop 0
	global_load_lds_dwordx4 v[162:163], off
	s_waitcnt vmcnt(8)
	s_waitcnt lgkmcnt(0)
	s_barrier
	s_waitcnt lgkmcnt(0)
	v_mfma_f32_16x16x32_bf16 v[128:131], v[140:143], v[188:191], v[128:131]
	v_mfma_f32_16x16x32_bf16 v[124:127], v[154:157], v[188:191], v[124:127]
	v_mfma_f32_16x16x32_bf16 v[112:115], v[140:143], v[196:199], v[112:115]
	v_mfma_f32_16x16x32_bf16 v[108:111], v[154:157], v[196:199], v[108:111]
	v_mfma_f32_16x16x32_bf16 v[96:99], v[140:143], v[204:207], v[96:99]
	v_mfma_f32_16x16x32_bf16 v[92:95], v[154:157], v[204:207], v[92:95]
	v_mfma_f32_16x16x32_bf16 v[78:81], v[140:143], v[212:215], v[78:81]
	v_mfma_f32_16x16x32_bf16 v[74:77], v[154:157], v[212:215], v[74:77]
	v_mfma_f32_16x16x32_bf16 v[128:131], v[144:147], v[192:195], v[128:131]
	v_mfma_f32_16x16x32_bf16 v[124:127], v[158:161], v[192:195], v[124:127]
	v_mfma_f32_16x16x32_bf16 v[112:115], v[144:147], v[200:203], v[112:115]
	v_mfma_f32_16x16x32_bf16 v[108:111], v[158:161], v[200:203], v[108:111]
	v_mfma_f32_16x16x32_bf16 v[96:99], v[144:147], v[208:211], v[96:99]
	v_mfma_f32_16x16x32_bf16 v[92:95], v[158:161], v[208:211], v[92:95]
	v_mfma_f32_16x16x32_bf16 v[78:81], v[144:147], v[234:237], v[78:81]
	v_mfma_f32_16x16x32_bf16 v[74:77], v[158:161], v[234:237], v[74:77]
	v_mfma_f32_16x16x32_bf16 v[120:123], v[172:175], v[188:191], v[120:123]
	v_mfma_f32_16x16x32_bf16 v[116:119], v[180:183], v[188:191], v[116:119]
	v_mfma_f32_16x16x32_bf16 v[104:107], v[172:175], v[196:199], v[104:107]
	v_mfma_f32_16x16x32_bf16 v[100:103], v[180:183], v[196:199], v[100:103]
	v_mfma_f32_16x16x32_bf16 v[86:89], v[172:175], v[204:207], v[86:89]
	v_mfma_f32_16x16x32_bf16 v[82:85], v[180:183], v[204:207], v[82:85]
	v_mfma_f32_16x16x32_bf16 v[70:73], v[172:175], v[212:215], v[70:73]
	v_mfma_f32_16x16x32_bf16 v[66:69], v[180:183], v[212:215], v[66:69]
	v_mfma_f32_16x16x32_bf16 v[120:123], v[176:179], v[192:195], v[120:123]
	v_mfma_f32_16x16x32_bf16 v[116:119], v[184:187], v[192:195], v[116:119]
	v_mfma_f32_16x16x32_bf16 v[104:107], v[176:179], v[200:203], v[104:107]
	v_mfma_f32_16x16x32_bf16 v[100:103], v[184:187], v[200:203], v[100:103]
	v_mfma_f32_16x16x32_bf16 v[86:89], v[176:179], v[208:211], v[86:89]
	v_mfma_f32_16x16x32_bf16 v[82:85], v[184:187], v[208:211], v[82:85]
	v_mfma_f32_16x16x32_bf16 v[70:73], v[176:179], v[234:237], v[70:73]
	v_mfma_f32_16x16x32_bf16 v[66:69], v[184:187], v[234:237], v[66:69]
	s_barrier
	s_add_i32 s45, s70, s62
	v_lshl_add_u64 v[162:163], s[56:57], 0, v[132:133]
	s_mov_b32 m0, s45
	ds_read_b128 v[188:191], v152 offset:16384
	ds_read_b128 v[192:195], v152 offset:17408
	ds_read_b128 v[196:199], v152 offset:18432
	ds_read_b128 v[200:203], v152 offset:19456
	ds_read_b128 v[204:207], v152 offset:20480
	ds_read_b128 v[208:211], v152 offset:21504
	ds_read_b128 v[212:215], v152 offset:22528
	ds_read_b128 v[234:237], v152 offset:23552
	global_load_lds_dwordx4 v[162:163], off
	s_add_i32 m0, s45, 0x2000
	s_add_u32 s70, s56, 0x80000
	v_lshl_add_u64 v[164:165], s[56:57], 0, v[134:135]
	s_addc_u32 s71, s57, 0
	s_add_i32 s37, s37, s62
	global_load_lds_dwordx4 v[164:165], off
	v_lshl_add_u64 v[166:167], s[70:71], 0, v[132:133]
	s_mov_b32 m0, s37
	v_lshl_add_u64 v[216:217], s[58:59], 0, v[134:135]
	global_load_lds_dwordx4 v[166:167], off
	v_lshl_add_u64 v[166:167], s[70:71], 0, v[134:135]
	s_add_i32 m0, s37, 0x2000
	s_nop 0
	global_load_lds_dwordx4 v[166:167], off
	v_lshl_add_u64 v[166:167], s[58:59], 0, v[132:133]
	s_mov_b32 m0, s63
	s_nop 0
	global_load_lds_dwordx4 v[166:167], off
	s_mov_b32 m0, s0
	s_nop 0
	global_load_lds_dwordx4 v[216:217], off
	s_waitcnt vmcnt(8)
	s_waitcnt lgkmcnt(0)
	s_barrier
; #define PG8_STAGE(bufoff, gbase, voff) do { _Pragma("unroll") for (int _i = 0; _i < 2; ++_i) \
;         __builtin_amdgcn_global_load_lds((const unsigned*)((const char*)(gbase) + (voff)[_i]), (LAS unsigned*)(lds + (bufoff) + ldsw + _i * 8192), 16, 0, 0); } while (0)
; #define PG8_LDA(dst, b, h) do { _Pragma("unroll") for (int m = 0; m < 4; ++m) _Pragma("unroll") for (int k = 0; k < 2; ++k) dst[m][k] = *(const LAS bf16x8*)(lds + PG8_SA(b, h) + aoff + m * 2048 + k * 1024); } while (0)
; #define PG8_LDB(dst, b, h) do { _Pragma("unroll") for (int n = 0; n < 2; ++n) _Pragma("unroll") for (int k = 0; k < 2; ++k) dst[n][k] = *(const LAS bf16x8*)(lds + PG8_SB(b, h) + boff + n * 2048 + k * 1024); } while (0)
; #define PG8_MMA(ai, bj, At, Bt) do { __builtin_amdgcn_s_setprio(1); _Pragma("unroll") for (int m = 0; m < 4; ++m) _Pragma("unroll") for (int n = 0; n < 2; ++n) _Pragma("unroll") for (int k = 0; k < 2; ++k) \
;         acc[ai][bj][m][n] = __builtin_amdgcn_mfma_f32_16x16x32_bf16(Bt[n][k], At[m][k], acc[ai][bj][m][n], 0, 0, 0); __builtin_amdgcn_s_setprio(0); } while (0)
; #define PG8_WAIT_V(n) asm volatile("s_waitcnt vmcnt(" #n ")" ::: "memory")
; #define PG8_WAIT_L(n) asm volatile("s_waitcnt lgkmcnt(" #n ")" ::: "memory")
; #define PG8_BAR __builtin_amdgcn_s_barrier()
; #define PG8_SCHED __builtin_amdgcn_sched_barrier(0)
; template <class Epi, class Sched, bool ALIGN_EPI = true, bool SP2 = true>
; __device__ __forceinline__ void gemm_phase(LAS unsigned char* lds, const Dims g, const Sched& S, const Epi& E) {
;     ...
;             PG8_WAIT_V(8); PG8_WAIT_L(0); PG8_BAR; PG8_MMA(1, 0, At, B0); PG8_MMA(1, 1, At, B1); PG8_BAR; PG8_SCHED;
;             PG8_LDB(B0, 1, 0); PG8_LDB(B1, 1, 1); PG8_SCHED; PG8_LDA(At, 1, 0); PG8_STAGE(PG8_SA(0, 1), a2 + hstepA, voffA);
;             PG8_WAIT_V(8); PG8_WAIT_L(0); PG8_BAR; PG8_MMA(0, 0, At, B0); PG8_MMA(0, 1, At, B1); PG8_BAR; PG8_SCHED;
;             PG8_LDA(At, 1, 1); PG8_STAGE(PG8_SB(1, 0), b3, voffB); PG8_STAGE(PG8_SB(1, 1), b3 + hstepB, voffB); PG8_STAGE(PG8_SA(1, 0), a3, voffA);
	s_waitcnt lgkmcnt(0)
	v_mfma_f32_16x16x32_bf16 v[62:65], v[140:143], v[188:191], v[62:65]
	v_mfma_f32_16x16x32_bf16 v[58:61], v[154:157], v[188:191], v[58:61]
	v_mfma_f32_16x16x32_bf16 v[46:49], v[140:143], v[196:199], v[46:49]
	v_mfma_f32_16x16x32_bf16 v[42:45], v[154:157], v[196:199], v[42:45]
	v_mfma_f32_16x16x32_bf16 v[30:33], v[140:143], v[204:207], v[30:33]
	v_mfma_f32_16x16x32_bf16 v[26:29], v[154:157], v[204:207], v[26:29]
	v_mfma_f32_16x16x32_bf16 v[14:17], v[140:143], v[212:215], v[14:17]
	v_mfma_f32_16x16x32_bf16 v[10:13], v[154:157], v[212:215], v[10:13]
	v_mfma_f32_16x16x32_bf16 v[62:65], v[144:147], v[192:195], v[62:65]
	v_mfma_f32_16x16x32_bf16 v[58:61], v[158:161], v[192:195], v[58:61]
	v_mfma_f32_16x16x32_bf16 v[46:49], v[144:147], v[200:203], v[46:49]
	v_mfma_f32_16x16x32_bf16 v[42:45], v[158:161], v[200:203], v[42:45]
	v_mfma_f32_16x16x32_bf16 v[30:33], v[144:147], v[208:211], v[30:33]
	v_mfma_f32_16x16x32_bf16 v[26:29], v[158:161], v[208:211], v[26:29]
	v_mfma_f32_16x16x32_bf16 v[14:17], v[144:147], v[234:237], v[14:17]
	v_mfma_f32_16x16x32_bf16 v[10:13], v[158:161], v[234:237], v[10:13]
	v_mfma_f32_16x16x32_bf16 v[54:57], v[172:175], v[188:191], v[54:57]
	v_mfma_f32_16x16x32_bf16 v[50:53], v[180:183], v[188:191], v[50:53]
	v_mfma_f32_16x16x32_bf16 v[38:41], v[172:175], v[196:199], v[38:41]
	v_mfma_f32_16x16x32_bf16 v[34:37], v[180:183], v[196:199], v[34:37]
	v_mfma_f32_16x16x32_bf16 v[22:25], v[172:175], v[204:207], v[22:25]
	v_mfma_f32_16x16x32_bf16 v[18:21], v[180:183], v[204:207], v[18:21]
	v_mfma_f32_16x16x32_bf16 v[6:9], v[172:175], v[212:215], v[6:9]
	v_mfma_f32_16x16x32_bf16 v[2:5], v[180:183], v[212:215], v[2:5]
	v_mfma_f32_16x16x32_bf16 v[54:57], v[176:179], v[192:195], v[54:57]
	v_mfma_f32_16x16x32_bf16 v[50:53], v[184:187], v[192:195], v[50:53]
	v_mfma_f32_16x16x32_bf16 v[38:41], v[176:179], v[200:203], v[38:41]
	v_mfma_f32_16x16x32_bf16 v[34:37], v[184:187], v[200:203], v[34:37]
	v_mfma_f32_16x16x32_bf16 v[22:25], v[176:179], v[208:211], v[22:25]
	v_mfma_f32_16x16x32_bf16 v[18:21], v[184:187], v[208:211], v[18:21]
	v_mfma_f32_16x16x32_bf16 v[6:9], v[176:179], v[234:237], v[6:9]
	v_mfma_f32_16x16x32_bf16 v[2:5], v[184:187], v[234:237], v[2:5]
	s_barrier
	s_add_i32 s37, 0, 0x18000
	v_add_u32_e32 v90, s37, v150
	s_add_i32 s45, 0, 0x1c000
	ds_read_b128 v[140:143], v90
	ds_read_b128 v[144:147], v90 offset:1024
	ds_read_b128 v[154:157], v90 offset:2048
	ds_read_b128 v[158:161], v90 offset:3072
	v_add_u32_e32 v90, s45, v150
	ds_read_b128 v[172:175], v90
	ds_read_b128 v[176:179], v90 offset:1024
	ds_read_b128 v[180:183], v90 offset:2048
	ds_read_b128 v[184:187], v90 offset:3072
	s_add_u32 s58, s58, 0x80000
	s_addc_u32 s59, s59, 0
	s_mov_b32 m0, s33
	v_lshl_add_u64 v[238:239], s[58:59], 0, v[132:133]
	ds_read_b128 v[188:191], v152 offset:32768
	ds_read_b128 v[192:195], v152 offset:33792
	ds_read_b128 v[196:199], v152 offset:34816
	ds_read_b128 v[200:203], v152 offset:35840
	ds_read_b128 v[204:207], v152 offset:36864
	ds_read_b128 v[208:211], v152 offset:37888
	ds_read_b128 v[212:215], v152 offset:38912
	ds_read_b128 v[234:237], v152 offset:39936
	global_load_lds_dwordx4 v[238:239], off
	v_lshl_add_u64 v[238:239], s[58:59], 0, v[134:135]
	s_mov_b32 m0, s64
	s_nop 0
	global_load_lds_dwordx4 v[238:239], off
	s_waitcnt vmcnt(8)
	s_waitcnt lgkmcnt(0)
	s_barrier
	s_waitcnt lgkmcnt(0)
	v_mfma_f32_16x16x32_bf16 v[128:131], v[140:143], v[188:191], v[128:131]
	v_mfma_f32_16x16x32_bf16 v[124:127], v[154:157], v[188:191], v[124:127]
	v_mfma_f32_16x16x32_bf16 v[112:115], v[140:143], v[196:199], v[112:115]
	v_mfma_f32_16x16x32_bf16 v[108:111], v[154:157], v[196:199], v[108:111]
	v_mfma_f32_16x16x32_bf16 v[96:99], v[140:143], v[204:207], v[96:99]
	v_mfma_f32_16x16x32_bf16 v[92:95], v[154:157], v[204:207], v[92:95]
	v_mfma_f32_16x16x32_bf16 v[78:81], v[140:143], v[212:215], v[78:81]
	v_mfma_f32_16x16x32_bf16 v[74:77], v[154:157], v[212:215], v[74:77]
	v_mfma_f32_16x16x32_bf16 v[128:131], v[144:147], v[192:195], v[128:131]
	v_mfma_f32_16x16x32_bf16 v[124:127], v[158:161], v[192:195], v[124:127]
	v_mfma_f32_16x16x32_bf16 v[112:115], v[144:147], v[200:203], v[112:115]
	v_mfma_f32_16x16x32_bf16 v[108:111], v[158:161], v[200:203], v[108:111]
	v_mfma_f32_16x16x32_bf16 v[96:99], v[144:147], v[208:211], v[96:99]
	v_mfma_f32_16x16x32_bf16 v[92:95], v[158:161], v[208:211], v[92:95]
	v_mfma_f32_16x16x32_bf16 v[78:81], v[144:147], v[234:237], v[78:81]
	v_mfma_f32_16x16x32_bf16 v[74:77], v[158:161], v[234:237], v[74:77]
	v_mfma_f32_16x16x32_bf16 v[120:123], v[172:175], v[188:191], v[120:123]
	v_mfma_f32_16x16x32_bf16 v[116:119], v[180:183], v[188:191], v[116:119]
	v_mfma_f32_16x16x32_bf16 v[104:107], v[172:175], v[196:199], v[104:107]
	v_mfma_f32_16x16x32_bf16 v[100:103], v[180:183], v[196:199], v[100:103]
	v_mfma_f32_16x16x32_bf16 v[86:89], v[172:175], v[204:207], v[86:89]
	v_mfma_f32_16x16x32_bf16 v[82:85], v[180:183], v[204:207], v[82:85]
	v_mfma_f32_16x16x32_bf16 v[70:73], v[172:175], v[212:215], v[70:73]
	v_mfma_f32_16x16x32_bf16 v[66:69], v[180:183], v[212:215], v[66:69]
	v_mfma_f32_16x16x32_bf16 v[120:123], v[176:179], v[192:195], v[120:123]
	v_mfma_f32_16x16x32_bf16 v[116:119], v[184:187], v[192:195], v[116:119]
	v_mfma_f32_16x16x32_bf16 v[104:107], v[176:179], v[200:203], v[104:107]
	v_mfma_f32_16x16x32_bf16 v[100:103], v[184:187], v[200:203], v[100:103]
	v_mfma_f32_16x16x32_bf16 v[86:89], v[176:179], v[208:211], v[86:89]
	v_mfma_f32_16x16x32_bf16 v[82:85], v[184:187], v[208:211], v[82:85]
	v_mfma_f32_16x16x32_bf16 v[70:73], v[176:179], v[234:237], v[70:73]
	v_mfma_f32_16x16x32_bf16 v[66:69], v[184:187], v[234:237], v[66:69]
	s_barrier
; #define PG8_STAGE(bufoff, gbase, voff) do { _Pragma("unroll") for (int _i = 0; _i < 2; ++_i) \
;         __builtin_amdgcn_global_load_lds((const unsigned*)((const char*)(gbase) + (voff)[_i]), (LAS unsigned*)(lds + (bufoff) + ldsw + _i * 8192), 16, 0, 0); } while (0)
; #define PG8_LDA(dst, b, h) do { _Pragma("unroll") for (int m = 0; m < 4; ++m) _Pragma("unroll") for (int k = 0; k < 2; ++k) dst[m][k] = *(const LAS bf16x8*)(lds + PG8_SA(b, h) + aoff + m * 2048 + k * 1024); } while (0)
; #define PG8_MMA(ai, bj, At, Bt) do { __builtin_amdgcn_s_setprio(1); _Pragma("unroll") for (int m = 0; m < 4; ++m) _Pragma("unroll") for (int n = 0; n < 2; ++n) _Pragma("unroll") for (int k = 0; k < 2; ++k) \
;         acc[ai][bj][m][n] = __builtin_amdgcn_mfma_f32_16x16x32_bf16(Bt[n][k], At[m][k], acc[ai][bj][m][n], 0, 0, 0); __builtin_amdgcn_s_setprio(0); } while (0)
; #define PG8_WAIT_V(n) asm volatile("s_waitcnt vmcnt(" #n ")" ::: "memory")
; #define PG8_WAIT_L(n) asm volatile("s_waitcnt lgkmcnt(" #n ")" ::: "memory")
; #define PG8_BAR __builtin_amdgcn_s_barrier()
; #define PG8_SCHED __builtin_amdgcn_sched_barrier(0)
; template <class Epi, class Sched, bool ALIGN_EPI = true, bool SP2 = true>
; __device__ __forceinline__ void gemm_phase(LAS unsigned char* lds, const Dims g, const Sched& S, const Epi& E) {
;     ...
;             PG8_LDA(At, 1, 1); PG8_STAGE(PG8_SB(1, 0), b3, voffB); PG8_STAGE(PG8_SB(1, 1), b3 + hstepB, voffB); PG8_STAGE(PG8_SA(1, 0), a3, voffA);
;             PG8_WAIT_V(8); PG8_WAIT_L(0); PG8_BAR; PG8_MMA(1, 0, At, B0); PG8_MMA(1, 1, At, B1); PG8_BAR; PG8_SCHED;
;     ...
;         if constexpr (ALIGN_EPI) { if (wr == 0) PG8_BAR; }
	s_add_i32 s37, s37, s62
	v_lshl_add_u64 v[162:163], v[162:163], 0, s[16:17]
	s_mov_b32 m0, s37
	ds_read_b128 v[188:191], v152 offset:49152
	ds_read_b128 v[192:195], v152 offset:50176
	ds_read_b128 v[196:199], v152 offset:51200
	ds_read_b128 v[200:203], v152 offset:52224
	ds_read_b128 v[204:207], v152 offset:53248
	ds_read_b128 v[208:211], v152 offset:54272
	ds_read_b128 v[212:215], v152 offset:55296
	ds_read_b128 v[234:237], v152 offset:56320
	global_load_lds_dwordx4 v[162:163], off
	s_add_i32 m0, s37, 0x2000
	s_add_u32 s56, s56, 0x80080
	v_lshl_add_u64 v[162:163], v[164:165], 0, s[16:17]
	s_addc_u32 s57, s57, 0
	s_add_i32 s37, s45, s62
	global_load_lds_dwordx4 v[162:163], off
	v_lshl_add_u64 v[162:163], s[56:57], 0, v[132:133]
	s_mov_b32 m0, s37
	s_nop 0
	global_load_lds_dwordx4 v[162:163], off
	v_lshl_add_u64 v[162:163], s[56:57], 0, v[134:135]
	s_add_i32 m0, s37, 0x2000
	s_nop 0
	global_load_lds_dwordx4 v[162:163], off
	v_lshl_add_u64 v[162:163], v[166:167], 0, s[16:17]
	s_mov_b32 m0, s1
	s_nop 0
	global_load_lds_dwordx4 v[162:163], off
	v_lshl_add_u64 v[162:163], v[216:217], 0, s[16:17]
	s_mov_b32 m0, s65
	s_nop 0
	global_load_lds_dwordx4 v[162:163], off
	s_waitcnt vmcnt(8)
	s_waitcnt lgkmcnt(0)
	s_barrier
	s_waitcnt lgkmcnt(0)
	v_mfma_f32_16x16x32_bf16 v[62:65], v[140:143], v[188:191], v[62:65]
	v_mfma_f32_16x16x32_bf16 v[58:61], v[154:157], v[188:191], v[58:61]
	v_mfma_f32_16x16x32_bf16 v[46:49], v[140:143], v[196:199], v[46:49]
	v_mfma_f32_16x16x32_bf16 v[42:45], v[154:157], v[196:199], v[42:45]
	v_mfma_f32_16x16x32_bf16 v[30:33], v[140:143], v[204:207], v[30:33]
	v_mfma_f32_16x16x32_bf16 v[26:29], v[154:157], v[204:207], v[26:29]
	v_mfma_f32_16x16x32_bf16 v[14:17], v[140:143], v[212:215], v[14:17]
	v_mfma_f32_16x16x32_bf16 v[10:13], v[154:157], v[212:215], v[10:13]
	v_mfma_f32_16x16x32_bf16 v[62:65], v[144:147], v[192:195], v[62:65]
	v_mfma_f32_16x16x32_bf16 v[58:61], v[158:161], v[192:195], v[58:61]
	v_mfma_f32_16x16x32_bf16 v[46:49], v[144:147], v[200:203], v[46:49]
	v_mfma_f32_16x16x32_bf16 v[42:45], v[158:161], v[200:203], v[42:45]
	v_mfma_f32_16x16x32_bf16 v[30:33], v[144:147], v[208:211], v[30:33]
	v_mfma_f32_16x16x32_bf16 v[26:29], v[158:161], v[208:211], v[26:29]
	v_mfma_f32_16x16x32_bf16 v[14:17], v[144:147], v[234:237], v[14:17]
	v_mfma_f32_16x16x32_bf16 v[10:13], v[158:161], v[234:237], v[10:13]
	v_mfma_f32_16x16x32_bf16 v[54:57], v[172:175], v[188:191], v[54:57]
	v_mfma_f32_16x16x32_bf16 v[50:53], v[180:183], v[188:191], v[50:53]
	v_mfma_f32_16x16x32_bf16 v[38:41], v[172:175], v[196:199], v[38:41]
	v_mfma_f32_16x16x32_bf16 v[34:37], v[180:183], v[196:199], v[34:37]
	v_mfma_f32_16x16x32_bf16 v[22:25], v[172:175], v[204:207], v[22:25]
	v_mfma_f32_16x16x32_bf16 v[18:21], v[180:183], v[204:207], v[18:21]
	v_mfma_f32_16x16x32_bf16 v[6:9], v[172:175], v[212:215], v[6:9]
	v_mfma_f32_16x16x32_bf16 v[2:5], v[180:183], v[212:215], v[2:5]
	v_mfma_f32_16x16x32_bf16 v[54:57], v[176:179], v[192:195], v[54:57]
	v_mfma_f32_16x16x32_bf16 v[50:53], v[184:187], v[192:195], v[50:53]
	v_mfma_f32_16x16x32_bf16 v[38:41], v[176:179], v[200:203], v[38:41]
	v_mfma_f32_16x16x32_bf16 v[34:37], v[184:187], v[200:203], v[34:37]
	v_mfma_f32_16x16x32_bf16 v[22:25], v[176:179], v[208:211], v[22:25]
	v_mfma_f32_16x16x32_bf16 v[18:21], v[184:187], v[208:211], v[18:21]
	v_mfma_f32_16x16x32_bf16 v[6:9], v[176:179], v[234:237], v[6:9]
	v_mfma_f32_16x16x32_bf16 v[2:5], v[184:187], v[234:237], v[2:5]
	s_barrier
	s_add_i32 s35, s35, 2
	s_add_u32 s54, s54, 0x100
	s_addc_u32 s55, s55, 0
	s_add_u32 s2, s2, 0x100
	s_addc_u32 s3, s3, 0
	s_cmp_gt_u32 s35, 29
	s_cbranch_scc0 .LBB0_1515
	s_and_b64 vcc, exec, s[28:29]
	s_cbranch_vccz .LBB0_1518
	s_barrier

; #define IN(k) (((PHMASK >> PHBIT(k)) & 1u) && lo <= (k) && (k) < hi)
; #define SEAM(k) do { if (IN(k) && IN((k) + 1)) xcd_barrier(bar); } while (0)
; #define DUP(bit) if constexpr (((PROBE_DUP >> (bit)) & 1u) != 0u)
; __global__ void __launch_bounds__(NTHR, 2) mk_fwd(ArgsV argsv) {
;     ...
;         if (IN(pb + 6)) { RUN_WOUT(WS_H); DUP(PB_WOUT) RUN_WOUT(WS_YR); } SEAM(pb + 6);
;         if (IN(pb + 7)) { { PH_BEGIN(); phase_router(a, l, lds, wave, lane, bid, G); } DUP(PB_ROUTER) { PH_BEGIN(); phase_router(a, l, lds, wave, lane, bid, G, true); } } SEAM(pb + 7);
.LBB0_1633:
	s_setprio 0
	s_cmp_le_i32 s76, s0
	s_cselect_b64 s[2:3], -1, 0
	s_cmp_lt_i32 s0, s77
	s_cselect_b64 s[0:1], -1, 0
	s_and_b64 s[0:1], s[2:3], s[0:1]
	s_mov_b64 s[2:3], -1
	s_and_b64 vcc, exec, s[0:1]
	s_cbranch_vccnz .LBB0_1635
	v_readlane_b32 s0, v255, 32
	s_add_i32 s0, s0, 9
	s_mov_b64 s[2:3], 0
